# in-proj tile-13 epilogue: forget-gate log-sigmoid computed once per unit spread over all 64 lanes via permlane swaps (same f32 log1pf sequence), 12 instances instead of 48
# speedup vs baseline: 1.0136x; 1.0118x over previous
; #define PG8_PACK8(y0, y1) (u32x4){cvt_pk_bf16((y0)[0], (y0)[1]), cvt_pk_bf16((y0)[2], (y0)[3]), cvt_pk_bf16((y1)[0], (y1)[1]), cvt_pk_bf16((y1)[2], (y1)[3])}
;     __device__ __forceinline__ void operator()(const f32x4 (&acc)[2][2][4][2], const Unit& u, int ui, int wr, int wc, int fr, int fq) const {
;     ...
;         } else {
; #pragma unroll
;             for (int ai = 0; ai < 2; ++ai)
; #pragma unroll
;                 for (int m = 0; m < 4; ++m) {
;                     const unsigned row = row0 + ai * HALF + m * 16; const float rs = rsp[ai * HALF + m * 16];
; #pragma unroll
;                     for (int bj = 0; bj < 2; ++bj) {
;                         const f32x4 y0 = acc[ai][bj][m][0] * rs, y1 = acc[ai][bj][m][1] * rs;
;                         if (pn == 12 || bj == 0) {
;                             const unsigned gcol = (unsigned)((pn == 12 ? 0 : 256) + 128 * bj + 32 * wc + 8 * fq);
;                             f32x4 s0, s1;
; #pragma unroll
;                             for (int e = 0; e < 4; ++e) { s0[e] = __builtin_amdgcn_rcpf(1.0f + __builtin_amdgcn_exp2f(y0[e] * -1.4426950408889634f)); s1[e] = __builtin_amdgcn_rcpf(1.0f + __builtin_amdgcn_exp2f(y1[e] * -1.4426950408889634f)); }
;                             *(u32x4*)(ws + E_GF + (size_t)((row * 384u + gcol) * 2u)) = PG8_PACK8(s0, s1);
;                         } else if (wc == 0 && fq == 0) {
;                             float z[6] = {y0[0], y0[1], y0[2], y0[3], y1[0], y1[1]};
; #pragma unroll
;                             for (int e = 0; e < 6; ++e) { const float zz = z[e] + bfg[e]; z[e] = fminf(zz, 0.f) - log1pf(__expf(-fabsf(zz))); }
;                             float* lp = (float*)(ws + E_LS) + (size_t)row;
; #pragma unroll
;                             for (int e = 0; e < 6; ++e) lp[(size_t)(e * 32768u)] = z[e];
.LBB0_559:
	s_cmp_eq_u32 s4, s42
	s_cselect_b32 s19, 0, 0x400
	v_lshl_add_u32 v158, s4, 8, v163
	v_add_u32_e32 v160, s19, v181
	s_cmp_gt_i32 s26, 7
	s_mov_b64 s[28:29], -1
	s_cbranch_scc0 .LBB0_613
	s_cmp_lt_u32 s26, 12
	s_cbranch_scc1 .LBB0_610
	ds_read_b32 v140, v160
	s_cmp_lg_u32 s26, 12
	s_cselect_b64 s[28:29], -1, 0
	s_cmp_eq_u32 s26, 12
	s_cselect_b32 s19, 0, 0x100
	s_waitcnt lgkmcnt(0)
	v_pk_mul_f32 v[130:131], v[124:125], v[140:141] op_sel_hi:[1,0]
	v_pk_mul_f32 v[134:135], v[126:127], v[140:141] op_sel_hi:[1,0]
	v_pk_mul_f32 v[136:137], v[128:129], v[140:141] op_sel_hi:[1,0]
	v_mul_f32_e32 v130, 0xbfb8aa3b, v130
	v_mul_f32_e32 v0, 0xbfb8aa3b, v134
	v_mul_f32_e32 v134, 0xbfb8aa3b, v135
	v_mul_f32_e32 v135, 0xbfb8aa3b, v136
	v_exp_f32_e32 v130, v130
	v_mul_f32_e32 v136, 0xbfb8aa3b, v137
	v_pk_mul_f32 v[132:133], v[122:123], v[140:141] op_sel_hi:[1,0]
	v_exp_f32_e32 v0, v0
	v_exp_f32_e32 v136, v136
	v_mul_f32_e32 v131, 0xbfb8aa3b, v131
	v_mul_f32_e32 v132, 0xbfb8aa3b, v132
	v_exp_f32_e32 v134, v134
	v_mul_f32_e32 v133, 0xbfb8aa3b, v133
	v_exp_f32_e32 v135, v135
	v_exp_f32_e32 v131, v131
	v_exp_f32_e32 v132, v132
	v_exp_f32_e32 v133, v133
	v_add_f32_e32 v130, 1.0, v130
	v_or_b32_e32 v161, s19, v237
	s_movk_i32 s19, 0x180
	v_add_f32_e32 v0, 1.0, v0
	v_rcp_f32_e32 v137, v130
	v_add_f32_e32 v130, 1.0, v136
	v_mul_lo_u32 v144, v158, s19
	v_rcp_f32_e32 v0, v0
	v_add_f32_e32 v134, 1.0, v134
	v_add_f32_e32 v135, 1.0, v135
	v_rcp_f32_e32 v136, v130
	v_add_f32_e32 v130, 1.0, v131
	v_add_f32_e32 v132, 1.0, v132
	v_rcp_f32_e32 v134, v134
	v_add_f32_e32 v133, 1.0, v133
	v_rcp_f32_e32 v135, v135
	v_rcp_f32_e32 v138, v130
	v_cvt_pk_bf16_f32 v130, v0, v134
	v_add_lshl_u32 v0, v144, v161, 1
	v_rcp_f32_e32 v132, v132
	v_rcp_f32_e32 v133, v133
	v_cvt_pk_bf16_f32 v131, v135, v136
	v_lshl_add_u64 v[134:135], s[10:11], 0, v[0:1]
	v_cvt_pk_bf16_f32 v132, v132, v133
	v_cvt_pk_bf16_f32 v133, v137, v138
	flat_store_dwordx4 v[134:135], v[130:133]
	v_pk_mul_f32 v[134:135], v[120:121], v[140:141] op_sel_hi:[1,0]
	v_pk_mul_f32 v[138:139], v[118:119], v[140:141] op_sel_hi:[1,0]
	v_pk_mul_f32 v[136:137], v[116:117], v[140:141] op_sel_hi:[1,0]
	v_pk_mul_f32 v[140:141], v[114:115], v[140:141] op_sel_hi:[1,0]
	s_mov_b64 s[30:31], -1
	s_and_b64 vcc, exec, s[28:29]
	s_cbranch_vccz .LBB0_565
	s_and_saveexec_b64 s[30:31], s[34:35]
	s_cbranch_execz .LBB0_564
.LBB0_564:
	s_or_b64 exec, exec, s[30:31]
	s_mov_b64 s[30:31], 0

; #define PG8_PACK8(y0, y1) (u32x4){cvt_pk_bf16((y0)[0], (y0)[1]), cvt_pk_bf16((y0)[2], (y0)[3]), cvt_pk_bf16((y1)[0], (y1)[1]), cvt_pk_bf16((y1)[2], (y1)[3])}
;     __device__ __forceinline__ void operator()(const f32x4 (&acc)[2][2][4][2], const Unit& u, int ui, int wr, int wc, int fr, int fq) const {
;     ...
;         } else {
; #pragma unroll
;             for (int ai = 0; ai < 2; ++ai)
; #pragma unroll
;                 for (int m = 0; m < 4; ++m) {
;                     const unsigned row = row0 + ai * HALF + m * 16; const float rs = rsp[ai * HALF + m * 16];
; #pragma unroll
;                     for (int bj = 0; bj < 2; ++bj) {
;                         const f32x4 y0 = acc[ai][bj][m][0] * rs, y1 = acc[ai][bj][m][1] * rs;
;                         if (pn == 12 || bj == 0) {
;                             const unsigned gcol = (unsigned)((pn == 12 ? 0 : 256) + 128 * bj + 32 * wc + 8 * fq);
;                             f32x4 s0, s1;
; #pragma unroll
;                             for (int e = 0; e < 4; ++e) { s0[e] = __builtin_amdgcn_rcpf(1.0f + __builtin_amdgcn_exp2f(y0[e] * -1.4426950408889634f)); s1[e] = __builtin_amdgcn_rcpf(1.0f + __builtin_amdgcn_exp2f(y1[e] * -1.4426950408889634f)); }
;                             *(u32x4*)(ws + E_GF + (size_t)((row * 384u + gcol) * 2u)) = PG8_PACK8(s0, s1);
;                         } else if (wc == 0 && fq == 0) {
;                             float z[6] = {y0[0], y0[1], y0[2], y0[3], y1[0], y1[1]};
; #pragma unroll
;                             for (int e = 0; e < 6; ++e) { const float zz = z[e] + bfg[e]; z[e] = fminf(zz, 0.f) - log1pf(__expf(-fabsf(zz))); }
;                             float* lp = (float*)(ws + E_LS) + (size_t)row;
; #pragma unroll
;                             for (int e = 0; e < 6; ++e) lp[(size_t)(e * 32768u)] = z[e];
.LBB0_567:
	ds_read_b32 v140, v160 offset:64
	v_add_u32_e32 v159, 0x1800, v144
	s_andn2_b64 vcc, exec, s[28:29]
	s_waitcnt lgkmcnt(0)
	v_pk_mul_f32 v[130:131], v[106:107], v[140:141] op_sel_hi:[1,0]
	v_pk_mul_f32 v[132:133], v[110:111], v[140:141] op_sel_hi:[1,0]
	v_mul_f32_e32 v130, 0xbfb8aa3b, v130
	v_mul_f32_e32 v0, 0xbfb8aa3b, v132
	v_exp_f32_e32 v130, v130
	v_mul_f32_e32 v132, 0xbfb8aa3b, v133
	v_exp_f32_e32 v132, v132
	v_pk_mul_f32 v[134:135], v[108:109], v[140:141] op_sel_hi:[1,0]
	v_pk_mul_f32 v[136:137], v[112:113], v[140:141] op_sel_hi:[1,0]
	v_add_f32_e32 v130, 1.0, v130
	v_mul_f32_e32 v131, 0xbfb8aa3b, v131
	v_exp_f32_e32 v131, v131
	v_rcp_f32_e32 v133, v130
	v_add_f32_e32 v130, 1.0, v132
	v_mul_f32_e32 v132, 0xbfb8aa3b, v136
	v_mul_f32_e32 v134, 0xbfb8aa3b, v134
	v_exp_f32_e32 v132, v132
	v_exp_f32_e32 v134, v134
	v_add_f32_e32 v131, 1.0, v131
	v_exp_f32_e32 v0, v0
	v_rcp_f32_e32 v136, v131
	v_add_f32_e32 v131, 1.0, v132
	v_add_f32_e32 v132, 1.0, v134
	v_mul_f32_e32 v134, 0xbfb8aa3b, v137
	v_mul_f32_e32 v135, 0xbfb8aa3b, v135
	v_exp_f32_e32 v134, v134
	v_exp_f32_e32 v135, v135
	v_add_f32_e32 v0, 1.0, v0
	v_rcp_f32_e32 v0, v0
	v_rcp_f32_e32 v130, v130
	v_rcp_f32_e32 v137, v132
	v_add_f32_e32 v132, 1.0, v134
	v_add_f32_e32 v134, 1.0, v135
	v_rcp_f32_e32 v131, v131
	v_rcp_f32_e32 v132, v132
	v_rcp_f32_e32 v134, v134
	v_cvt_pk_bf16_f32 v130, v0, v130
	v_add_lshl_u32 v0, v159, v161, 1
	v_cvt_pk_bf16_f32 v131, v131, v132
	v_cvt_pk_bf16_f32 v132, v133, v136
	v_cvt_pk_bf16_f32 v133, v137, v134
	v_lshl_add_u64 v[134:135], s[10:11], 0, v[0:1]
	flat_store_dwordx4 v[134:135], v[130:133]
	v_pk_mul_f32 v[134:135], v[104:105], v[140:141] op_sel_hi:[1,0]
	v_pk_mul_f32 v[138:139], v[102:103], v[140:141] op_sel_hi:[1,0]
	v_cndmask_b32_e64 v130, 0, 1, s[28:29]
	v_pk_mul_f32 v[136:137], v[100:101], v[140:141] op_sel_hi:[1,0]
	v_pk_mul_f32 v[140:141], v[98:99], v[140:141] op_sel_hi:[1,0]
	v_cmp_ne_u32_e64 s[40:41], 1, v130
	s_mov_b64 s[28:29], -1
	s_cbranch_vccnz .LBB0_571
	s_and_saveexec_b64 s[28:29], s[34:35]
	s_cbranch_execz .LBB0_570
.LBB0_570:
	s_or_b64 exec, exec, s[28:29]
	s_mov_b64 s[28:29], 0

; #define PG8_PACK8(y0, y1) (u32x4){cvt_pk_bf16((y0)[0], (y0)[1]), cvt_pk_bf16((y0)[2], (y0)[3]), cvt_pk_bf16((y1)[0], (y1)[1]), cvt_pk_bf16((y1)[2], (y1)[3])}
;     __device__ __forceinline__ void operator()(const f32x4 (&acc)[2][2][4][2], const Unit& u, int ui, int wr, int wc, int fr, int fq) const {
;     ...
;         } else {
; #pragma unroll
;             for (int ai = 0; ai < 2; ++ai)
; #pragma unroll
;                 for (int m = 0; m < 4; ++m) {
;                     const unsigned row = row0 + ai * HALF + m * 16; const float rs = rsp[ai * HALF + m * 16];
; #pragma unroll
;                     for (int bj = 0; bj < 2; ++bj) {
;                         const f32x4 y0 = acc[ai][bj][m][0] * rs, y1 = acc[ai][bj][m][1] * rs;
;                         if (pn == 12 || bj == 0) {
;                             const unsigned gcol = (unsigned)((pn == 12 ? 0 : 256) + 128 * bj + 32 * wc + 8 * fq);
;                             f32x4 s0, s1;
; #pragma unroll
;                             for (int e = 0; e < 4; ++e) { s0[e] = __builtin_amdgcn_rcpf(1.0f + __builtin_amdgcn_exp2f(y0[e] * -1.4426950408889634f)); s1[e] = __builtin_amdgcn_rcpf(1.0f + __builtin_amdgcn_exp2f(y1[e] * -1.4426950408889634f)); }
;                             *(u32x4*)(ws + E_GF + (size_t)((row * 384u + gcol) * 2u)) = PG8_PACK8(s0, s1);
;                         } else if (wc == 0 && fq == 0) {
;                             float z[6] = {y0[0], y0[1], y0[2], y0[3], y1[0], y1[1]};
; #pragma unroll
;                             for (int e = 0; e < 6; ++e) { const float zz = z[e] + bfg[e]; z[e] = fminf(zz, 0.f) - log1pf(__expf(-fabsf(zz))); }
;                             float* lp = (float*)(ws + E_LS) + (size_t)row;
; #pragma unroll
;                             for (int e = 0; e < 6; ++e) lp[(size_t)(e * 32768u)] = z[e];
.LBB0_573:
	ds_read_b32 v140, v160 offset:128
	v_add_u32_e32 v159, 0x1800, v159
	s_and_b64 vcc, exec, s[40:41]
	s_mov_b64 s[28:29], -1
	s_waitcnt lgkmcnt(0)
	v_pk_mul_f32 v[130:131], v[90:91], v[140:141] op_sel_hi:[1,0]
	v_pk_mul_f32 v[132:133], v[94:95], v[140:141] op_sel_hi:[1,0]
	v_mul_f32_e32 v130, 0xbfb8aa3b, v130
	v_mul_f32_e32 v0, 0xbfb8aa3b, v132
	v_exp_f32_e32 v130, v130
	v_mul_f32_e32 v132, 0xbfb8aa3b, v133
	v_exp_f32_e32 v132, v132
	v_pk_mul_f32 v[134:135], v[92:93], v[140:141] op_sel_hi:[1,0]
	v_pk_mul_f32 v[136:137], v[96:97], v[140:141] op_sel_hi:[1,0]
	v_add_f32_e32 v130, 1.0, v130
	v_mul_f32_e32 v131, 0xbfb8aa3b, v131
	v_exp_f32_e32 v131, v131
	v_rcp_f32_e32 v133, v130
	v_add_f32_e32 v130, 1.0, v132
	v_mul_f32_e32 v132, 0xbfb8aa3b, v136
	v_mul_f32_e32 v134, 0xbfb8aa3b, v134
	v_exp_f32_e32 v132, v132
	v_exp_f32_e32 v134, v134
	v_add_f32_e32 v131, 1.0, v131
	v_exp_f32_e32 v0, v0
	v_rcp_f32_e32 v136, v131
	v_add_f32_e32 v131, 1.0, v132
	v_add_f32_e32 v132, 1.0, v134
	v_mul_f32_e32 v134, 0xbfb8aa3b, v137
	v_mul_f32_e32 v135, 0xbfb8aa3b, v135
	v_exp_f32_e32 v134, v134
	v_exp_f32_e32 v135, v135
	v_add_f32_e32 v0, 1.0, v0
	v_rcp_f32_e32 v0, v0
	v_rcp_f32_e32 v130, v130
	v_rcp_f32_e32 v137, v132
	v_add_f32_e32 v132, 1.0, v134
	v_add_f32_e32 v134, 1.0, v135
	v_rcp_f32_e32 v131, v131
	v_rcp_f32_e32 v132, v132
	v_rcp_f32_e32 v134, v134
	v_cvt_pk_bf16_f32 v130, v0, v130
	v_add_lshl_u32 v0, v159, v161, 1
	v_cvt_pk_bf16_f32 v131, v131, v132
	v_cvt_pk_bf16_f32 v132, v133, v136
	v_cvt_pk_bf16_f32 v133, v137, v134
	v_lshl_add_u64 v[134:135], s[10:11], 0, v[0:1]
	flat_store_dwordx4 v[134:135], v[130:133]
	v_pk_mul_f32 v[134:135], v[88:89], v[140:141] op_sel_hi:[1,0]
	v_pk_mul_f32 v[138:139], v[86:87], v[140:141] op_sel_hi:[1,0]
	v_pk_mul_f32 v[136:137], v[84:85], v[140:141] op_sel_hi:[1,0]
	v_pk_mul_f32 v[140:141], v[82:83], v[140:141] op_sel_hi:[1,0]
	s_cbranch_vccnz .LBB0_577
	s_and_saveexec_b64 s[28:29], s[34:35]
	s_cbranch_execz .LBB0_576
.LBB0_576:
	s_or_b64 exec, exec, s[28:29]
	s_mov_b64 s[28:29], 0

; #define PG8_PACK8(y0, y1) (u32x4){cvt_pk_bf16((y0)[0], (y0)[1]), cvt_pk_bf16((y0)[2], (y0)[3]), cvt_pk_bf16((y1)[0], (y1)[1]), cvt_pk_bf16((y1)[2], (y1)[3])}
;     __device__ __forceinline__ void operator()(const f32x4 (&acc)[2][2][4][2], const Unit& u, int ui, int wr, int wc, int fr, int fq) const {
;     ...
;         } else {
; #pragma unroll
;             for (int ai = 0; ai < 2; ++ai)
; #pragma unroll
;                 for (int m = 0; m < 4; ++m) {
;                     const unsigned row = row0 + ai * HALF + m * 16; const float rs = rsp[ai * HALF + m * 16];
; #pragma unroll
;                     for (int bj = 0; bj < 2; ++bj) {
;                         const f32x4 y0 = acc[ai][bj][m][0] * rs, y1 = acc[ai][bj][m][1] * rs;
;                         if (pn == 12 || bj == 0) {
;                             const unsigned gcol = (unsigned)((pn == 12 ? 0 : 256) + 128 * bj + 32 * wc + 8 * fq);
;                             f32x4 s0, s1;
; #pragma unroll
;                             for (int e = 0; e < 4; ++e) { s0[e] = __builtin_amdgcn_rcpf(1.0f + __builtin_amdgcn_exp2f(y0[e] * -1.4426950408889634f)); s1[e] = __builtin_amdgcn_rcpf(1.0f + __builtin_amdgcn_exp2f(y1[e] * -1.4426950408889634f)); }
;                             *(u32x4*)(ws + E_GF + (size_t)((row * 384u + gcol) * 2u)) = PG8_PACK8(s0, s1);
;                         } else if (wc == 0 && fq == 0) {
;                             float z[6] = {y0[0], y0[1], y0[2], y0[3], y1[0], y1[1]};
; #pragma unroll
;                             for (int e = 0; e < 6; ++e) { const float zz = z[e] + bfg[e]; z[e] = fminf(zz, 0.f) - log1pf(__expf(-fabsf(zz))); }
;                             float* lp = (float*)(ws + E_LS) + (size_t)row;
; #pragma unroll
;                             for (int e = 0; e < 6; ++e) lp[(size_t)(e * 32768u)] = z[e];
.LBB0_579:
	ds_read_b32 v140, v160 offset:192
	v_add_u32_e32 v159, 0x1800, v159
	s_and_b64 vcc, exec, s[40:41]
	s_mov_b64 s[28:29], -1
	s_waitcnt lgkmcnt(0)
	v_pk_mul_f32 v[130:131], v[74:75], v[140:141] op_sel_hi:[1,0]
	v_pk_mul_f32 v[132:133], v[78:79], v[140:141] op_sel_hi:[1,0]
	v_mul_f32_e32 v130, 0xbfb8aa3b, v130
	v_mul_f32_e32 v0, 0xbfb8aa3b, v132
	v_exp_f32_e32 v130, v130
	v_mul_f32_e32 v132, 0xbfb8aa3b, v133
	v_exp_f32_e32 v132, v132
	v_pk_mul_f32 v[134:135], v[76:77], v[140:141] op_sel_hi:[1,0]
	v_pk_mul_f32 v[136:137], v[80:81], v[140:141] op_sel_hi:[1,0]
	v_add_f32_e32 v130, 1.0, v130
	v_mul_f32_e32 v131, 0xbfb8aa3b, v131
	v_exp_f32_e32 v131, v131
	v_rcp_f32_e32 v133, v130
	v_add_f32_e32 v130, 1.0, v132
	v_mul_f32_e32 v132, 0xbfb8aa3b, v136
	v_mul_f32_e32 v134, 0xbfb8aa3b, v134
	v_exp_f32_e32 v132, v132
	v_exp_f32_e32 v134, v134
	v_add_f32_e32 v131, 1.0, v131
	v_exp_f32_e32 v0, v0
	v_rcp_f32_e32 v136, v131
	v_add_f32_e32 v131, 1.0, v132
	v_add_f32_e32 v132, 1.0, v134
	v_mul_f32_e32 v134, 0xbfb8aa3b, v137
	v_mul_f32_e32 v135, 0xbfb8aa3b, v135
	v_exp_f32_e32 v134, v134
	v_exp_f32_e32 v135, v135
	v_add_f32_e32 v0, 1.0, v0
	v_rcp_f32_e32 v0, v0
	v_rcp_f32_e32 v130, v130
	v_rcp_f32_e32 v137, v132
	v_add_f32_e32 v132, 1.0, v134
	v_add_f32_e32 v134, 1.0, v135
	v_rcp_f32_e32 v131, v131
	v_rcp_f32_e32 v132, v132
	v_rcp_f32_e32 v134, v134
	v_cvt_pk_bf16_f32 v130, v0, v130
	v_add_lshl_u32 v0, v159, v161, 1
	v_cvt_pk_bf16_f32 v131, v131, v132
	v_cvt_pk_bf16_f32 v132, v133, v136
	v_cvt_pk_bf16_f32 v133, v137, v134
	v_lshl_add_u64 v[134:135], s[10:11], 0, v[0:1]
	flat_store_dwordx4 v[134:135], v[130:133]
	v_pk_mul_f32 v[134:135], v[72:73], v[140:141] op_sel_hi:[1,0]
	v_pk_mul_f32 v[138:139], v[70:71], v[140:141] op_sel_hi:[1,0]
	v_pk_mul_f32 v[136:137], v[68:69], v[140:141] op_sel_hi:[1,0]
	v_pk_mul_f32 v[140:141], v[66:67], v[140:141] op_sel_hi:[1,0]
	s_cbranch_vccnz .LBB0_583
	s_and_saveexec_b64 s[28:29], s[34:35]
	s_cbranch_execz .LBB0_582
.LBB0_582:
	s_or_b64 exec, exec, s[28:29]
	s_mov_b64 s[28:29], 0

; #define PG8_PACK8(y0, y1) (u32x4){cvt_pk_bf16((y0)[0], (y0)[1]), cvt_pk_bf16((y0)[2], (y0)[3]), cvt_pk_bf16((y1)[0], (y1)[1]), cvt_pk_bf16((y1)[2], (y1)[3])}
;     __device__ __forceinline__ void operator()(const f32x4 (&acc)[2][2][4][2], const Unit& u, int ui, int wr, int wc, int fr, int fq) const {
;     ...
;         } else {
; #pragma unroll
;             for (int ai = 0; ai < 2; ++ai)
; #pragma unroll
;                 for (int m = 0; m < 4; ++m) {
;                     const unsigned row = row0 + ai * HALF + m * 16; const float rs = rsp[ai * HALF + m * 16];
; #pragma unroll
;                     for (int bj = 0; bj < 2; ++bj) {
;                         const f32x4 y0 = acc[ai][bj][m][0] * rs, y1 = acc[ai][bj][m][1] * rs;
;                         if (pn == 12 || bj == 0) {
;                             const unsigned gcol = (unsigned)((pn == 12 ? 0 : 256) + 128 * bj + 32 * wc + 8 * fq);
;                             f32x4 s0, s1;
; #pragma unroll
;                             for (int e = 0; e < 4; ++e) { s0[e] = __builtin_amdgcn_rcpf(1.0f + __builtin_amdgcn_exp2f(y0[e] * -1.4426950408889634f)); s1[e] = __builtin_amdgcn_rcpf(1.0f + __builtin_amdgcn_exp2f(y1[e] * -1.4426950408889634f)); }
;                             *(u32x4*)(ws + E_GF + (size_t)((row * 384u + gcol) * 2u)) = PG8_PACK8(s0, s1);
;                         } else if (wc == 0 && fq == 0) {
;                             float z[6] = {y0[0], y0[1], y0[2], y0[3], y1[0], y1[1]};
; #pragma unroll
;                             for (int e = 0; e < 6; ++e) { const float zz = z[e] + bfg[e]; z[e] = fminf(zz, 0.f) - log1pf(__expf(-fabsf(zz))); }
;                             float* lp = (float*)(ws + E_LS) + (size_t)row;
; #pragma unroll
;                             for (int e = 0; e < 6; ++e) lp[(size_t)(e * 32768u)] = z[e];
.LBB0_585:
	ds_read_b32 v140, v160 offset:512
	v_add_u32_e32 v159, 0x7800, v159
	s_and_b64 vcc, exec, s[40:41]
	s_mov_b64 s[28:29], -1
	s_waitcnt lgkmcnt(0)
	v_pk_mul_f32 v[130:131], v[58:59], v[140:141] op_sel_hi:[1,0]
	v_pk_mul_f32 v[132:133], v[62:63], v[140:141] op_sel_hi:[1,0]
	v_mul_f32_e32 v130, 0xbfb8aa3b, v130
	v_mul_f32_e32 v0, 0xbfb8aa3b, v132
	v_exp_f32_e32 v130, v130
	v_mul_f32_e32 v132, 0xbfb8aa3b, v133
	v_exp_f32_e32 v132, v132
	v_pk_mul_f32 v[134:135], v[60:61], v[140:141] op_sel_hi:[1,0]
	v_pk_mul_f32 v[136:137], v[64:65], v[140:141] op_sel_hi:[1,0]
	v_add_f32_e32 v130, 1.0, v130
	v_mul_f32_e32 v131, 0xbfb8aa3b, v131
	v_exp_f32_e32 v131, v131
	v_rcp_f32_e32 v133, v130
	v_add_f32_e32 v130, 1.0, v132
	v_mul_f32_e32 v132, 0xbfb8aa3b, v136
	v_mul_f32_e32 v134, 0xbfb8aa3b, v134
	v_exp_f32_e32 v132, v132
	v_exp_f32_e32 v134, v134
	v_add_f32_e32 v131, 1.0, v131
	v_exp_f32_e32 v0, v0
	v_rcp_f32_e32 v136, v131
	v_add_f32_e32 v131, 1.0, v132
	v_add_f32_e32 v132, 1.0, v134
	v_mul_f32_e32 v134, 0xbfb8aa3b, v137
	v_mul_f32_e32 v135, 0xbfb8aa3b, v135
	v_exp_f32_e32 v134, v134
	v_exp_f32_e32 v135, v135
	v_add_f32_e32 v0, 1.0, v0
	v_rcp_f32_e32 v0, v0
	v_rcp_f32_e32 v130, v130
	v_rcp_f32_e32 v137, v132
	v_add_f32_e32 v132, 1.0, v134
	v_add_f32_e32 v134, 1.0, v135
	v_rcp_f32_e32 v131, v131
	v_rcp_f32_e32 v132, v132
	v_rcp_f32_e32 v134, v134
	v_cvt_pk_bf16_f32 v130, v0, v130
	v_add_lshl_u32 v0, v159, v161, 1
	v_cvt_pk_bf16_f32 v131, v131, v132
	v_cvt_pk_bf16_f32 v132, v133, v136
	v_cvt_pk_bf16_f32 v133, v137, v134
	v_lshl_add_u64 v[134:135], s[10:11], 0, v[0:1]
	flat_store_dwordx4 v[134:135], v[130:133]
	v_pk_mul_f32 v[134:135], v[56:57], v[140:141] op_sel_hi:[1,0]
	v_pk_mul_f32 v[138:139], v[54:55], v[140:141] op_sel_hi:[1,0]
	v_pk_mul_f32 v[136:137], v[52:53], v[140:141] op_sel_hi:[1,0]
	v_pk_mul_f32 v[140:141], v[50:51], v[140:141] op_sel_hi:[1,0]
	s_cbranch_vccnz .LBB0_589
	s_and_saveexec_b64 s[28:29], s[34:35]
	s_cbranch_execz .LBB0_588
.LBB0_588:
	s_or_b64 exec, exec, s[28:29]
	s_mov_b64 s[28:29], 0

; #define PG8_PACK8(y0, y1) (u32x4){cvt_pk_bf16((y0)[0], (y0)[1]), cvt_pk_bf16((y0)[2], (y0)[3]), cvt_pk_bf16((y1)[0], (y1)[1]), cvt_pk_bf16((y1)[2], (y1)[3])}
;     __device__ __forceinline__ void operator()(const f32x4 (&acc)[2][2][4][2], const Unit& u, int ui, int wr, int wc, int fr, int fq) const {
;     ...
;         } else {
; #pragma unroll
;             for (int ai = 0; ai < 2; ++ai)
; #pragma unroll
;                 for (int m = 0; m < 4; ++m) {
;                     const unsigned row = row0 + ai * HALF + m * 16; const float rs = rsp[ai * HALF + m * 16];
; #pragma unroll
;                     for (int bj = 0; bj < 2; ++bj) {
;                         const f32x4 y0 = acc[ai][bj][m][0] * rs, y1 = acc[ai][bj][m][1] * rs;
;                         if (pn == 12 || bj == 0) {
;                             const unsigned gcol = (unsigned)((pn == 12 ? 0 : 256) + 128 * bj + 32 * wc + 8 * fq);
;                             f32x4 s0, s1;
; #pragma unroll
;                             for (int e = 0; e < 4; ++e) { s0[e] = __builtin_amdgcn_rcpf(1.0f + __builtin_amdgcn_exp2f(y0[e] * -1.4426950408889634f)); s1[e] = __builtin_amdgcn_rcpf(1.0f + __builtin_amdgcn_exp2f(y1[e] * -1.4426950408889634f)); }
;                             *(u32x4*)(ws + E_GF + (size_t)((row * 384u + gcol) * 2u)) = PG8_PACK8(s0, s1);
;                         } else if (wc == 0 && fq == 0) {
;                             float z[6] = {y0[0], y0[1], y0[2], y0[3], y1[0], y1[1]};
; #pragma unroll
;                             for (int e = 0; e < 6; ++e) { const float zz = z[e] + bfg[e]; z[e] = fminf(zz, 0.f) - log1pf(__expf(-fabsf(zz))); }
;                             float* lp = (float*)(ws + E_LS) + (size_t)row;
; #pragma unroll
;                             for (int e = 0; e < 6; ++e) lp[(size_t)(e * 32768u)] = z[e];
.LBB0_591:
	ds_read_b32 v140, v160 offset:576
	v_add_u32_e32 v159, 0x1800, v159
	s_and_b64 vcc, exec, s[40:41]
	s_mov_b64 s[28:29], -1
	s_waitcnt lgkmcnt(0)
	v_pk_mul_f32 v[130:131], v[42:43], v[140:141] op_sel_hi:[1,0]
	v_pk_mul_f32 v[132:133], v[46:47], v[140:141] op_sel_hi:[1,0]
	v_mul_f32_e32 v130, 0xbfb8aa3b, v130
	v_mul_f32_e32 v0, 0xbfb8aa3b, v132
	v_exp_f32_e32 v130, v130
	v_mul_f32_e32 v132, 0xbfb8aa3b, v133
	v_exp_f32_e32 v132, v132
	v_pk_mul_f32 v[134:135], v[44:45], v[140:141] op_sel_hi:[1,0]
	v_pk_mul_f32 v[136:137], v[48:49], v[140:141] op_sel_hi:[1,0]
	v_add_f32_e32 v130, 1.0, v130
	v_mul_f32_e32 v131, 0xbfb8aa3b, v131
	v_exp_f32_e32 v131, v131
	v_rcp_f32_e32 v133, v130
	v_add_f32_e32 v130, 1.0, v132
	v_mul_f32_e32 v132, 0xbfb8aa3b, v136
	v_mul_f32_e32 v134, 0xbfb8aa3b, v134
	v_exp_f32_e32 v132, v132
	v_exp_f32_e32 v134, v134
	v_add_f32_e32 v131, 1.0, v131
	v_exp_f32_e32 v0, v0
	v_rcp_f32_e32 v136, v131
	v_add_f32_e32 v131, 1.0, v132
	v_add_f32_e32 v132, 1.0, v134
	v_mul_f32_e32 v134, 0xbfb8aa3b, v137
	v_mul_f32_e32 v135, 0xbfb8aa3b, v135
	v_exp_f32_e32 v134, v134
	v_exp_f32_e32 v135, v135
	v_add_f32_e32 v0, 1.0, v0
	v_rcp_f32_e32 v0, v0
	v_rcp_f32_e32 v130, v130
	v_rcp_f32_e32 v137, v132
	v_add_f32_e32 v132, 1.0, v134
	v_add_f32_e32 v134, 1.0, v135
	v_rcp_f32_e32 v131, v131
	v_rcp_f32_e32 v132, v132
	v_rcp_f32_e32 v134, v134
	v_cvt_pk_bf16_f32 v130, v0, v130
	v_add_lshl_u32 v0, v159, v161, 1
	v_cvt_pk_bf16_f32 v131, v131, v132
	v_cvt_pk_bf16_f32 v132, v133, v136
	v_cvt_pk_bf16_f32 v133, v137, v134
	v_lshl_add_u64 v[134:135], s[10:11], 0, v[0:1]
	flat_store_dwordx4 v[134:135], v[130:133]
	v_pk_mul_f32 v[134:135], v[40:41], v[140:141] op_sel_hi:[1,0]
	v_pk_mul_f32 v[138:139], v[38:39], v[140:141] op_sel_hi:[1,0]
	v_pk_mul_f32 v[136:137], v[36:37], v[140:141] op_sel_hi:[1,0]
	v_pk_mul_f32 v[140:141], v[34:35], v[140:141] op_sel_hi:[1,0]
	s_cbranch_vccnz .LBB0_595
	s_and_saveexec_b64 s[28:29], s[34:35]
	s_cbranch_execz .LBB0_594
.LBB0_594:
	s_or_b64 exec, exec, s[28:29]
	s_mov_b64 s[28:29], 0

; #define PG8_PACK8(y0, y1) (u32x4){cvt_pk_bf16((y0)[0], (y0)[1]), cvt_pk_bf16((y0)[2], (y0)[3]), cvt_pk_bf16((y1)[0], (y1)[1]), cvt_pk_bf16((y1)[2], (y1)[3])}
;     __device__ __forceinline__ void operator()(const f32x4 (&acc)[2][2][4][2], const Unit& u, int ui, int wr, int wc, int fr, int fq) const {
;     ...
;         } else {
; #pragma unroll
;             for (int ai = 0; ai < 2; ++ai)
; #pragma unroll
;                 for (int m = 0; m < 4; ++m) {
;                     const unsigned row = row0 + ai * HALF + m * 16; const float rs = rsp[ai * HALF + m * 16];
; #pragma unroll
;                     for (int bj = 0; bj < 2; ++bj) {
;                         const f32x4 y0 = acc[ai][bj][m][0] * rs, y1 = acc[ai][bj][m][1] * rs;
;                         if (pn == 12 || bj == 0) {
;                             const unsigned gcol = (unsigned)((pn == 12 ? 0 : 256) + 128 * bj + 32 * wc + 8 * fq);
;                             f32x4 s0, s1;
; #pragma unroll
;                             for (int e = 0; e < 4; ++e) { s0[e] = __builtin_amdgcn_rcpf(1.0f + __builtin_amdgcn_exp2f(y0[e] * -1.4426950408889634f)); s1[e] = __builtin_amdgcn_rcpf(1.0f + __builtin_amdgcn_exp2f(y1[e] * -1.4426950408889634f)); }
;                             *(u32x4*)(ws + E_GF + (size_t)((row * 384u + gcol) * 2u)) = PG8_PACK8(s0, s1);
;                         } else if (wc == 0 && fq == 0) {
;                             float z[6] = {y0[0], y0[1], y0[2], y0[3], y1[0], y1[1]};
; #pragma unroll
;                             for (int e = 0; e < 6; ++e) { const float zz = z[e] + bfg[e]; z[e] = fminf(zz, 0.f) - log1pf(__expf(-fabsf(zz))); }
;                             float* lp = (float*)(ws + E_LS) + (size_t)row;
; #pragma unroll
;                             for (int e = 0; e < 6; ++e) lp[(size_t)(e * 32768u)] = z[e];
.LBB0_597:
	ds_read_b32 v140, v160 offset:640
	v_add_u32_e32 v159, 0x1800, v159
	s_and_b64 vcc, exec, s[40:41]
	s_mov_b64 s[28:29], -1
	s_waitcnt lgkmcnt(0)
	v_pk_mul_f32 v[130:131], v[26:27], v[140:141] op_sel_hi:[1,0]
	v_pk_mul_f32 v[132:133], v[30:31], v[140:141] op_sel_hi:[1,0]
	v_mul_f32_e32 v130, 0xbfb8aa3b, v130
	v_mul_f32_e32 v0, 0xbfb8aa3b, v132
	v_exp_f32_e32 v130, v130
	v_mul_f32_e32 v132, 0xbfb8aa3b, v133
	v_exp_f32_e32 v132, v132
	v_pk_mul_f32 v[134:135], v[28:29], v[140:141] op_sel_hi:[1,0]
	v_pk_mul_f32 v[136:137], v[32:33], v[140:141] op_sel_hi:[1,0]
	v_add_f32_e32 v130, 1.0, v130
	v_mul_f32_e32 v131, 0xbfb8aa3b, v131
	v_exp_f32_e32 v131, v131
	v_rcp_f32_e32 v133, v130
	v_add_f32_e32 v130, 1.0, v132
	v_mul_f32_e32 v132, 0xbfb8aa3b, v136
	v_mul_f32_e32 v134, 0xbfb8aa3b, v134
	v_exp_f32_e32 v132, v132
	v_exp_f32_e32 v134, v134
	v_add_f32_e32 v131, 1.0, v131
	v_exp_f32_e32 v0, v0
	v_rcp_f32_e32 v136, v131
	v_add_f32_e32 v131, 1.0, v132
	v_add_f32_e32 v132, 1.0, v134
	v_mul_f32_e32 v134, 0xbfb8aa3b, v137
	v_mul_f32_e32 v135, 0xbfb8aa3b, v135
	v_exp_f32_e32 v134, v134
	v_exp_f32_e32 v135, v135
	v_add_f32_e32 v0, 1.0, v0
	v_rcp_f32_e32 v0, v0
	v_rcp_f32_e32 v130, v130
	v_rcp_f32_e32 v137, v132
	v_add_f32_e32 v132, 1.0, v134
	v_add_f32_e32 v134, 1.0, v135
	v_rcp_f32_e32 v131, v131
	v_rcp_f32_e32 v132, v132
	v_rcp_f32_e32 v134, v134
	v_cvt_pk_bf16_f32 v130, v0, v130
	v_add_lshl_u32 v0, v159, v161, 1
	v_cvt_pk_bf16_f32 v131, v131, v132
	v_cvt_pk_bf16_f32 v132, v133, v136
	v_cvt_pk_bf16_f32 v133, v137, v134
	v_lshl_add_u64 v[134:135], s[10:11], 0, v[0:1]
	flat_store_dwordx4 v[134:135], v[130:133]
	v_pk_mul_f32 v[134:135], v[24:25], v[140:141] op_sel_hi:[1,0]
	v_pk_mul_f32 v[138:139], v[22:23], v[140:141] op_sel_hi:[1,0]
	v_pk_mul_f32 v[136:137], v[20:21], v[140:141] op_sel_hi:[1,0]
	v_pk_mul_f32 v[140:141], v[18:19], v[140:141] op_sel_hi:[1,0]
	s_cbranch_vccnz .LBB0_601
	s_and_saveexec_b64 s[28:29], s[34:35]
	s_cbranch_execz .LBB0_600
.LBB0_600:
	s_or_b64 exec, exec, s[28:29]
	s_mov_b64 s[28:29], 0

; #define PG8_PACK8(y0, y1) (u32x4){cvt_pk_bf16((y0)[0], (y0)[1]), cvt_pk_bf16((y0)[2], (y0)[3]), cvt_pk_bf16((y1)[0], (y1)[1]), cvt_pk_bf16((y1)[2], (y1)[3])}
;     __device__ __forceinline__ void operator()(const f32x4 (&acc)[2][2][4][2], const Unit& u, int ui, int wr, int wc, int fr, int fq) const {
;     ...
;                     const unsigned row = row0 + ai * HALF + m * 16; const float rs = rsp[ai * HALF + m * 16];
; #pragma unroll
;                     for (int bj = 0; bj < 2; ++bj) {
;                         const f32x4 y0 = acc[ai][bj][m][0] * rs, y1 = acc[ai][bj][m][1] * rs;
;                         if (pn == 12 || bj == 0) {
;                             const unsigned gcol = (unsigned)((pn == 12 ? 0 : 256) + 128 * bj + 32 * wc + 8 * fq);
;                             f32x4 s0, s1;
; #pragma unroll
;                             for (int e = 0; e < 4; ++e) { s0[e] = __builtin_amdgcn_rcpf(1.0f + __builtin_amdgcn_exp2f(y0[e] * -1.4426950408889634f)); s1[e] = __builtin_amdgcn_rcpf(1.0f + __builtin_amdgcn_exp2f(y1[e] * -1.4426950408889634f)); }
;                             *(u32x4*)(ws + E_GF + (size_t)((row * 384u + gcol) * 2u)) = PG8_PACK8(s0, s1);
;                         } else if (wc == 0 && fq == 0) {
;                             float z[6] = {y0[0], y0[1], y0[2], y0[3], y1[0], y1[1]};
; #pragma unroll
;                             for (int e = 0; e < 6; ++e) { const float zz = z[e] + bfg[e]; z[e] = fminf(zz, 0.f) - log1pf(__expf(-fabsf(zz))); }
;                             float* lp = (float*)(ws + E_LS) + (size_t)row;
; #pragma unroll
;                             for (int e = 0; e < 6; ++e) lp[(size_t)(e * 32768u)] = z[e];
.LBB0_603:
	ds_read_b32 v140, v160 offset:704
	v_add_u32_e32 v0, v159, v161
	s_and_b64 vcc, exec, s[40:41]
	s_mov_b64 s[28:29], -1
	s_waitcnt lgkmcnt(0)
	v_pk_mul_f32 v[130:131], v[10:11], v[140:141] op_sel_hi:[1,0]
	v_pk_mul_f32 v[132:133], v[14:15], v[140:141] op_sel_hi:[1,0]
	v_mul_f32_e32 v130, 0xbfb8aa3b, v130
	v_exp_f32_e32 v130, v130
	v_mul_f32_e32 v133, 0xbfb8aa3b, v133
	v_exp_f32_e32 v133, v133
	v_pk_mul_f32 v[134:135], v[12:13], v[140:141] op_sel_hi:[1,0]
	v_pk_mul_f32 v[136:137], v[16:17], v[140:141] op_sel_hi:[1,0]
	v_add_f32_e32 v130, 1.0, v130
	v_mul_f32_e32 v131, 0xbfb8aa3b, v131
	v_exp_f32_e32 v131, v131
	v_rcp_f32_e32 v138, v130
	v_add_f32_e32 v130, 1.0, v133
	v_mul_f32_e32 v133, 0xbfb8aa3b, v136
	v_mul_f32_e32 v134, 0xbfb8aa3b, v134
	v_exp_f32_e32 v133, v133
	v_exp_f32_e32 v134, v134
	v_add_f32_e32 v131, 1.0, v131
	v_rcp_f32_e32 v136, v131
	v_add_f32_e32 v131, 1.0, v133
	v_add_f32_e32 v133, 1.0, v134
	v_mul_f32_e32 v134, 0xbfb8aa3b, v137
	v_mul_f32_e32 v132, 0xbfb8aa3b, v132
	v_exp_f32_e32 v134, v134
	v_exp_f32_e32 v132, v132
	v_mul_f32_e32 v135, 0xbfb8aa3b, v135
	v_exp_f32_e32 v135, v135
	v_add_f32_e32 v134, 1.0, v134
	v_add_f32_e32 v132, 1.0, v132
	v_rcp_f32_e32 v130, v130
	v_rcp_f32_e32 v131, v131
	v_rcp_f32_e32 v134, v134
	v_rcp_f32_e32 v132, v132
	v_add_f32_e32 v135, 1.0, v135
	v_cvt_pk_bf16_f32 v130, v132, v130
	v_cvt_pk_bf16_f32 v131, v131, v134
	v_mov_b32_e32 v134, 0x3000
	v_rcp_f32_e32 v133, v133
	v_rcp_f32_e32 v135, v135
	v_lshl_add_u32 v0, v0, 1, v134
	v_cvt_pk_bf16_f32 v132, v138, v136
	v_cvt_pk_bf16_f32 v133, v133, v135
	v_lshl_add_u64 v[134:135], s[10:11], 0, v[0:1]
	flat_store_dwordx4 v[134:135], v[130:133]
	v_pk_mul_f32 v[134:135], v[8:9], v[140:141] op_sel_hi:[1,0]
	v_pk_mul_f32 v[138:139], v[6:7], v[140:141] op_sel_hi:[1,0]
	v_pk_mul_f32 v[136:137], v[4:5], v[140:141] op_sel_hi:[1,0]
	v_pk_mul_f32 v[140:141], v[2:3], v[140:141] op_sel_hi:[1,0]
	s_cbranch_vccnz .LBB0_607
	s_cmp_eq_u64 s[34:35], 0
	s_cbranch_scc1 .Lflg_done
	global_load_dwordx4 v[10:13], v1, s[6:7]
	global_load_dwordx2 v[14:15], v1, s[6:7] offset:16
	v_mbcnt_lo_u32_b32 v16, -1, 0
	v_mbcnt_hi_u32_b32 v16, -1, v16
	v_lshrrev_b32_e32 v17, 5, v16
	v_bfe_u32 v16, v16, 4, 1
	v_lshlrev_b32_e32 v17, 9, v17
	v_lshl_add_u32 v17, v16, 7, v17
	v_add_u32_e32 v16, v160, v17
	ds_read_b32 v26, v16
	ds_read_b32 v27, v16 offset:64
	v_lshl_add_u32 v28, v158, 2, v17
	s_mov_b32 s3, 0xbfb8aa3b
	s_mov_b32 s19, 0x3f2aaaab
	s_mov_b32 s21, 0x3f317218
	s_mov_b32 s27, 0x7f800000
	s_mov_b32 s33, 0x33800000
	v_permlane32_swap_b32_e32 v118, v54
	v_permlane32_swap_b32_e32 v119, v55
	v_permlane32_swap_b32_e32 v120, v56
	v_permlane32_swap_b32_e32 v121, v57
	v_permlane32_swap_b32_e32 v114, v50
	v_permlane32_swap_b32_e32 v115, v51
	v_permlane32_swap_b32_e32 v102, v38
	v_permlane32_swap_b32_e32 v103, v39
	v_permlane32_swap_b32_e32 v104, v40
	v_permlane32_swap_b32_e32 v105, v41
	v_permlane32_swap_b32_e32 v98, v34
	v_permlane32_swap_b32_e32 v99, v35
	v_permlane32_swap_b32_e32 v86, v22
	v_permlane32_swap_b32_e32 v87, v23
	v_permlane32_swap_b32_e32 v88, v24
	v_permlane32_swap_b32_e32 v89, v25
	v_permlane32_swap_b32_e32 v82, v18
	v_permlane32_swap_b32_e32 v83, v19
	v_permlane32_swap_b32_e32 v70, v6
	v_permlane32_swap_b32_e32 v71, v7
	v_permlane32_swap_b32_e32 v72, v8
	v_permlane32_swap_b32_e32 v73, v9
	v_permlane32_swap_b32_e32 v66, v2
	v_permlane32_swap_b32_e32 v67, v3
	s_nop 1
	v_permlane16_swap_b32_e32 v118, v86
	v_permlane16_swap_b32_e32 v119, v87
	v_permlane16_swap_b32_e32 v120, v88
	v_permlane16_swap_b32_e32 v121, v89
	v_permlane16_swap_b32_e32 v114, v82
	v_permlane16_swap_b32_e32 v115, v83
	v_permlane16_swap_b32_e32 v102, v70
	v_permlane16_swap_b32_e32 v103, v71
	v_permlane16_swap_b32_e32 v104, v72
	v_permlane16_swap_b32_e32 v105, v73
	v_permlane16_swap_b32_e32 v98, v66
	v_permlane16_swap_b32_e32 v99, v67
	s_waitcnt vmcnt(0) lgkmcnt(0)
	s_nop 1
	v_mul_f32_e32 v118, v118, v26
	v_add_f32_e32 v30, v118, v10
	v_min_f32_e32 v29, 0, v30
	v_mul_f32_e64 v30, |v30|, s3
	v_exp_f32_e32 v30, v30
	s_nop 0
	v_add_f32_e32 v32, 1.0, v30
	v_add_f32_e32 v31, -1.0, v32
	v_sub_f32_e32 v33, v31, v32
	v_add_f32_e32 v33, 1.0, v33
	v_sub_f32_e32 v31, v30, v31
	v_add_f32_e32 v33, v31, v33
	v_frexp_mant_f32_e32 v31, v32
	v_cvt_f64_f32_e32 v[42:43], v32
	v_cmp_gt_f32_e32 vcc, s19, v31
	v_frexp_exp_i32_f64_e32 v31, v[42:43]
	s_nop 0
	v_subbrev_co_u32_e32 v31, vcc, 0, v31, vcc
	v_sub_u32_e32 v42, 0, v31
	v_ldexp_f32 v32, v32, v42
	v_ldexp_f32 v33, v33, v42
	v_add_f32_e32 v42, -1.0, v32
	v_add_f32_e32 v43, 1.0, v42
	v_sub_f32_e32 v43, v32, v43
	v_add_f32_e32 v43, v33, v43
	v_add_f32_e32 v44, v42, v43
	v_sub_f32_e32 v42, v44, v42
	v_sub_f32_e32 v42, v43, v42
	v_add_f32_e32 v43, 1.0, v32
	v_add_f32_e32 v45, -1.0, v43
	v_sub_f32_e32 v32, v32, v45
	v_add_f32_e32 v32, v33, v32
	v_add_f32_e32 v33, v43, v32
	v_sub_f32_e32 v43, v33, v43
	v_sub_f32_e32 v32, v32, v43
	v_rcp_f32_e32 v43, v33
	v_cvt_f32_i32_e32 v31, v31
	v_cmp_neq_f32_e32 vcc, s27, v30
	v_mul_f32_e32 v45, v44, v43
	v_mul_f32_e32 v46, v33, v45
	v_fma_f32 v47, v45, v33, -v46
	v_fmac_f32_e32 v47, v45, v32
	v_add_f32_e32 v48, v46, v47
	v_sub_f32_e32 v49, v44, v48
	v_sub_f32_e32 v44, v44, v49
	v_sub_f32_e32 v46, v48, v46
	v_sub_f32_e32 v44, v44, v48
	v_add_f32_e32 v42, v42, v44
	v_sub_f32_e32 v44, v46, v47
	v_add_f32_e32 v42, v44, v42
	v_add_f32_e32 v44, v49, v42
	v_mul_f32_e32 v46, v43, v44
	v_mul_f32_e32 v47, v33, v46
	v_fma_f32 v33, v46, v33, -v47
	v_fmac_f32_e32 v33, v46, v32
	v_sub_f32_e32 v32, v49, v44
	v_add_f32_e32 v32, v42, v32
	v_add_f32_e32 v42, v47, v33
	v_sub_f32_e32 v48, v44, v42
	v_sub_f32_e32 v44, v44, v48
	v_sub_f32_e32 v47, v42, v47
;     __device__ __forceinline__ void operator()(const f32x4 (&acc)[2][2][4][2], const Unit& u, int ui, int wr, int wc, int fr, int fq) const {
;     ...
;                             float z[6] = {y0[0], y0[1], y0[2], y0[3], y1[0], y1[1]};
; #pragma unroll
;                             for (int e = 0; e < 6; ++e) { const float zz = z[e] + bfg[e]; z[e] = fminf(zz, 0.f) - log1pf(__expf(-fabsf(zz))); }
;                             float* lp = (float*)(ws + E_LS) + (size_t)row;
; #pragma unroll
;                             for (int e = 0; e < 6; ++e) lp[(size_t)(e * 32768u)] = z[e];
	v_sub_f32_e32 v42, v44, v42
	v_add_f32_e32 v32, v32, v42
	v_sub_f32_e32 v33, v47, v33
	v_add_f32_e32 v32, v33, v32
	v_add_f32_e32 v33, v45, v46
	v_add_f32_e32 v32, v48, v32
	v_sub_f32_e32 v42, v33, v45
	v_mul_f32_e32 v32, v43, v32
	v_sub_f32_e32 v42, v46, v42
	v_add_f32_e32 v32, v42, v32
	v_mul_f32_e32 v45, 0x3f317218, v31
	v_add_f32_e32 v42, v33, v32
	v_fma_f32 v46, v31, s21, -v45
	v_mul_f32_e32 v43, v42, v42
	v_fmac_f32_e32 v46, 0xb102e308, v31
	v_sub_f32_e32 v31, v42, v33
	v_fmamk_f32 v44, v43, 0x3e9b6dac, v217
	v_sub_f32_e32 v31, v32, v31
	v_add_f32_e32 v32, v45, v46
	v_fmaak_f32 v44, v43, v44, 0x3f2aaada
	v_sub_f32_e32 v33, v32, v45
	v_ldexp_f32 v45, v42, 1
	v_mul_f32_e32 v42, v42, v43
	v_mul_f32_e32 v42, v42, v44
	v_add_f32_e32 v43, v45, v42
	v_sub_f32_e32 v44, v43, v45
	v_ldexp_f32 v31, v31, 1
	v_sub_f32_e32 v42, v42, v44
	v_add_f32_e32 v31, v31, v42
	v_add_f32_e32 v42, v43, v31
	v_sub_f32_e32 v43, v42, v43
	v_sub_f32_e32 v31, v31, v43
	v_add_f32_e32 v43, v32, v42
	v_sub_f32_e32 v44, v43, v32
	v_sub_f32_e32 v45, v43, v44
	v_sub_f32_e32 v33, v46, v33
	v_sub_f32_e32 v32, v32, v45
	v_sub_f32_e32 v42, v42, v44
	v_add_f32_e32 v32, v42, v32
	v_add_f32_e32 v42, v33, v31
	v_sub_f32_e32 v44, v42, v33
	v_sub_f32_e32 v45, v42, v44
	v_sub_f32_e32 v33, v33, v45
	v_sub_f32_e32 v31, v31, v44
	v_add_f32_e32 v32, v42, v32
	v_add_f32_e32 v31, v31, v33
	v_add_f32_e32 v33, v43, v32
	v_sub_f32_e32 v42, v33, v43
	v_sub_f32_e32 v32, v32, v42
	v_add_f32_e32 v31, v31, v32
	v_add_f32_e32 v31, v33, v31
	v_cndmask_b32_e32 v31, v230, v31, vcc
	v_cmp_ngt_f32_e32 vcc, -1.0, v30
	s_nop 1
	v_cndmask_b32_e32 v31, v231, v31, vcc
	v_cmp_neq_f32_e32 vcc, -1.0, v30
	s_nop 1
	v_cndmask_b32_e32 v31, v226, v31, vcc
	v_cmp_lt_f32_e64 vcc, |v30|, s33
	s_nop 1
	v_cndmask_b32_e32 v30, v31, v30, vcc
	v_sub_f32_e32 v118, v29, v30
	v_mul_f32_e32 v119, v119, v26
	v_add_f32_e32 v30, v119, v11
	v_min_f32_e32 v29, 0, v30
	v_mul_f32_e64 v30, |v30|, s3
	v_exp_f32_e32 v30, v30
	s_nop 0
	v_add_f32_e32 v32, 1.0, v30
	v_add_f32_e32 v31, -1.0, v32
	v_sub_f32_e32 v33, v31, v32
	v_add_f32_e32 v33, 1.0, v33
	v_sub_f32_e32 v31, v30, v31
	v_add_f32_e32 v33, v31, v33
	v_frexp_mant_f32_e32 v31, v32
	v_cvt_f64_f32_e32 v[42:43], v32
	v_cmp_gt_f32_e32 vcc, s19, v31
	v_frexp_exp_i32_f64_e32 v31, v[42:43]
	s_nop 0
	v_subbrev_co_u32_e32 v31, vcc, 0, v31, vcc
	v_sub_u32_e32 v42, 0, v31
	v_ldexp_f32 v32, v32, v42
	v_ldexp_f32 v33, v33, v42
	v_add_f32_e32 v42, -1.0, v32
	v_add_f32_e32 v43, 1.0, v42
	v_sub_f32_e32 v43, v32, v43
	v_add_f32_e32 v43, v33, v43
	v_add_f32_e32 v44, v42, v43
	v_sub_f32_e32 v42, v44, v42
	v_sub_f32_e32 v42, v43, v42
	v_add_f32_e32 v43, 1.0, v32
	v_add_f32_e32 v45, -1.0, v43
	v_sub_f32_e32 v32, v32, v45
	v_add_f32_e32 v32, v33, v32
	v_add_f32_e32 v33, v43, v32
	v_sub_f32_e32 v43, v33, v43
	v_sub_f32_e32 v32, v32, v43
	v_rcp_f32_e32 v43, v33
	v_cvt_f32_i32_e32 v31, v31
	v_cmp_neq_f32_e32 vcc, s27, v30
	v_mul_f32_e32 v45, v44, v43
	v_mul_f32_e32 v46, v33, v45
	v_fma_f32 v47, v45, v33, -v46
	v_fmac_f32_e32 v47, v45, v32
	v_add_f32_e32 v48, v46, v47
	v_sub_f32_e32 v49, v44, v48
	v_sub_f32_e32 v44, v44, v49
	v_sub_f32_e32 v46, v48, v46
	v_sub_f32_e32 v44, v44, v48
	v_add_f32_e32 v42, v42, v44
	v_sub_f32_e32 v44, v46, v47
	v_add_f32_e32 v42, v44, v42
	v_add_f32_e32 v44, v49, v42
	v_mul_f32_e32 v46, v43, v44
	v_mul_f32_e32 v47, v33, v46
	v_fma_f32 v33, v46, v33, -v47
	v_fmac_f32_e32 v33, v46, v32
	v_sub_f32_e32 v32, v49, v44
	v_add_f32_e32 v32, v42, v32
	v_add_f32_e32 v42, v47, v33
	v_sub_f32_e32 v48, v44, v42
	v_sub_f32_e32 v44, v44, v48
	v_sub_f32_e32 v47, v42, v47
	v_sub_f32_e32 v42, v44, v42
	v_add_f32_e32 v32, v32, v42
	v_sub_f32_e32 v33, v47, v33
	v_add_f32_e32 v32, v33, v32
	v_add_f32_e32 v33, v45, v46
	v_add_f32_e32 v32, v48, v32
	v_sub_f32_e32 v42, v33, v45
	v_mul_f32_e32 v32, v43, v32
	v_sub_f32_e32 v42, v46, v42
	v_add_f32_e32 v32, v42, v32
	v_mul_f32_e32 v45, 0x3f317218, v31
	v_add_f32_e32 v42, v33, v32
	v_fma_f32 v46, v31, s21, -v45
	v_mul_f32_e32 v43, v42, v42
	v_fmac_f32_e32 v46, 0xb102e308, v31
	v_sub_f32_e32 v31, v42, v33
	v_fmamk_f32 v44, v43, 0x3e9b6dac, v217
	v_sub_f32_e32 v31, v32, v31
	v_add_f32_e32 v32, v45, v46
	v_fmaak_f32 v44, v43, v44, 0x3f2aaada
	v_sub_f32_e32 v33, v32, v45
	v_ldexp_f32 v45, v42, 1
	v_mul_f32_e32 v42, v42, v43
	v_mul_f32_e32 v42, v42, v44
	v_add_f32_e32 v43, v45, v42
	v_sub_f32_e32 v44, v43, v45
	v_ldexp_f32 v31, v31, 1
	v_sub_f32_e32 v42, v42, v44
	v_add_f32_e32 v31, v31, v42
	v_add_f32_e32 v42, v43, v31
	v_sub_f32_e32 v43, v42, v43
	v_sub_f32_e32 v31, v31, v43
	v_add_f32_e32 v43, v32, v42
	v_sub_f32_e32 v44, v43, v32
	v_sub_f32_e32 v45, v43, v44
	v_sub_f32_e32 v33, v46, v33
	v_sub_f32_e32 v32, v32, v45
	v_sub_f32_e32 v42, v42, v44
	v_add_f32_e32 v32, v42, v32
	v_add_f32_e32 v42, v33, v31
	v_sub_f32_e32 v44, v42, v33
	v_sub_f32_e32 v45, v42, v44
	v_sub_f32_e32 v33, v33, v45
	v_sub_f32_e32 v31, v31, v44
	v_add_f32_e32 v32, v42, v32
	v_add_f32_e32 v31, v31, v33
	v_add_f32_e32 v33, v43, v32
	v_sub_f32_e32 v42, v33, v43
	v_sub_f32_e32 v32, v32, v42
	v_add_f32_e32 v31, v31, v32
	v_add_f32_e32 v31, v33, v31
	v_cndmask_b32_e32 v31, v230, v31, vcc
	v_cmp_ngt_f32_e32 vcc, -1.0, v30
	s_nop 1
	v_cndmask_b32_e32 v31, v231, v31, vcc
	v_cmp_neq_f32_e32 vcc, -1.0, v30
	s_nop 1
	v_cndmask_b32_e32 v31, v226, v31, vcc
	v_cmp_lt_f32_e64 vcc, |v30|, s33
	s_nop 1
	v_cndmask_b32_e32 v30, v31, v30, vcc
	v_sub_f32_e32 v119, v29, v30
	v_mul_f32_e32 v120, v120, v26
	v_add_f32_e32 v30, v120, v12
	v_min_f32_e32 v29, 0, v30
	v_mul_f32_e64 v30, |v30|, s3
	v_exp_f32_e32 v30, v30
	s_nop 0
	v_add_f32_e32 v32, 1.0, v30
	v_add_f32_e32 v31, -1.0, v32
	v_sub_f32_e32 v33, v31, v32
;     __device__ __forceinline__ void operator()(const f32x4 (&acc)[2][2][4][2], const Unit& u, int ui, int wr, int wc, int fr, int fq) const {
;     ...
;                             float z[6] = {y0[0], y0[1], y0[2], y0[3], y1[0], y1[1]};
; #pragma unroll
;                             for (int e = 0; e < 6; ++e) { const float zz = z[e] + bfg[e]; z[e] = fminf(zz, 0.f) - log1pf(__expf(-fabsf(zz))); }
;                             float* lp = (float*)(ws + E_LS) + (size_t)row;
; #pragma unroll
;                             for (int e = 0; e < 6; ++e) lp[(size_t)(e * 32768u)] = z[e];
	v_add_f32_e32 v33, 1.0, v33
	v_sub_f32_e32 v31, v30, v31
	v_add_f32_e32 v33, v31, v33
	v_frexp_mant_f32_e32 v31, v32
	v_cvt_f64_f32_e32 v[42:43], v32
	v_cmp_gt_f32_e32 vcc, s19, v31
	v_frexp_exp_i32_f64_e32 v31, v[42:43]
	s_nop 0
	v_subbrev_co_u32_e32 v31, vcc, 0, v31, vcc
	v_sub_u32_e32 v42, 0, v31
	v_ldexp_f32 v32, v32, v42
	v_ldexp_f32 v33, v33, v42
	v_add_f32_e32 v42, -1.0, v32
	v_add_f32_e32 v43, 1.0, v42
	v_sub_f32_e32 v43, v32, v43
	v_add_f32_e32 v43, v33, v43
	v_add_f32_e32 v44, v42, v43
	v_sub_f32_e32 v42, v44, v42
	v_sub_f32_e32 v42, v43, v42
	v_add_f32_e32 v43, 1.0, v32
	v_add_f32_e32 v45, -1.0, v43
	v_sub_f32_e32 v32, v32, v45
	v_add_f32_e32 v32, v33, v32
	v_add_f32_e32 v33, v43, v32
	v_sub_f32_e32 v43, v33, v43
	v_sub_f32_e32 v32, v32, v43
	v_rcp_f32_e32 v43, v33
	v_cvt_f32_i32_e32 v31, v31
	v_cmp_neq_f32_e32 vcc, s27, v30
	v_mul_f32_e32 v45, v44, v43
	v_mul_f32_e32 v46, v33, v45
	v_fma_f32 v47, v45, v33, -v46
	v_fmac_f32_e32 v47, v45, v32
	v_add_f32_e32 v48, v46, v47
	v_sub_f32_e32 v49, v44, v48
	v_sub_f32_e32 v44, v44, v49
	v_sub_f32_e32 v46, v48, v46
	v_sub_f32_e32 v44, v44, v48
	v_add_f32_e32 v42, v42, v44
	v_sub_f32_e32 v44, v46, v47
	v_add_f32_e32 v42, v44, v42
	v_add_f32_e32 v44, v49, v42
	v_mul_f32_e32 v46, v43, v44
	v_mul_f32_e32 v47, v33, v46
	v_fma_f32 v33, v46, v33, -v47
	v_fmac_f32_e32 v33, v46, v32
	v_sub_f32_e32 v32, v49, v44
	v_add_f32_e32 v32, v42, v32
	v_add_f32_e32 v42, v47, v33
	v_sub_f32_e32 v48, v44, v42
	v_sub_f32_e32 v44, v44, v48
	v_sub_f32_e32 v47, v42, v47
	v_sub_f32_e32 v42, v44, v42
	v_add_f32_e32 v32, v32, v42
	v_sub_f32_e32 v33, v47, v33
	v_add_f32_e32 v32, v33, v32
	v_add_f32_e32 v33, v45, v46
	v_add_f32_e32 v32, v48, v32
	v_sub_f32_e32 v42, v33, v45
	v_mul_f32_e32 v32, v43, v32
	v_sub_f32_e32 v42, v46, v42
	v_add_f32_e32 v32, v42, v32
	v_mul_f32_e32 v45, 0x3f317218, v31
	v_add_f32_e32 v42, v33, v32
	v_fma_f32 v46, v31, s21, -v45
	v_mul_f32_e32 v43, v42, v42
	v_fmac_f32_e32 v46, 0xb102e308, v31
	v_sub_f32_e32 v31, v42, v33
	v_fmamk_f32 v44, v43, 0x3e9b6dac, v217
	v_sub_f32_e32 v31, v32, v31
	v_add_f32_e32 v32, v45, v46
	v_fmaak_f32 v44, v43, v44, 0x3f2aaada
	v_sub_f32_e32 v33, v32, v45
	v_ldexp_f32 v45, v42, 1
	v_mul_f32_e32 v42, v42, v43
	v_mul_f32_e32 v42, v42, v44
	v_add_f32_e32 v43, v45, v42
	v_sub_f32_e32 v44, v43, v45
	v_ldexp_f32 v31, v31, 1
	v_sub_f32_e32 v42, v42, v44
	v_add_f32_e32 v31, v31, v42
	v_add_f32_e32 v42, v43, v31
	v_sub_f32_e32 v43, v42, v43
	v_sub_f32_e32 v31, v31, v43
	v_add_f32_e32 v43, v32, v42
	v_sub_f32_e32 v44, v43, v32
	v_sub_f32_e32 v45, v43, v44
	v_sub_f32_e32 v33, v46, v33
	v_sub_f32_e32 v32, v32, v45
	v_sub_f32_e32 v42, v42, v44
	v_add_f32_e32 v32, v42, v32
	v_add_f32_e32 v42, v33, v31
	v_sub_f32_e32 v44, v42, v33
	v_sub_f32_e32 v45, v42, v44
	v_sub_f32_e32 v33, v33, v45
	v_sub_f32_e32 v31, v31, v44
	v_add_f32_e32 v32, v42, v32
	v_add_f32_e32 v31, v31, v33
	v_add_f32_e32 v33, v43, v32
	v_sub_f32_e32 v42, v33, v43
	v_sub_f32_e32 v32, v32, v42
	v_add_f32_e32 v31, v31, v32
	v_add_f32_e32 v31, v33, v31
	v_cndmask_b32_e32 v31, v230, v31, vcc
	v_cmp_ngt_f32_e32 vcc, -1.0, v30
	s_nop 1
	v_cndmask_b32_e32 v31, v231, v31, vcc
	v_cmp_neq_f32_e32 vcc, -1.0, v30
	s_nop 1
	v_cndmask_b32_e32 v31, v226, v31, vcc
	v_cmp_lt_f32_e64 vcc, |v30|, s33
	s_nop 1
	v_cndmask_b32_e32 v30, v31, v30, vcc
	v_sub_f32_e32 v120, v29, v30
	v_mul_f32_e32 v121, v121, v26
	v_add_f32_e32 v30, v121, v13
	v_min_f32_e32 v29, 0, v30
	v_mul_f32_e64 v30, |v30|, s3
	v_exp_f32_e32 v30, v30
	s_nop 0
	v_add_f32_e32 v32, 1.0, v30
	v_add_f32_e32 v31, -1.0, v32
	v_sub_f32_e32 v33, v31, v32
	v_add_f32_e32 v33, 1.0, v33
	v_sub_f32_e32 v31, v30, v31
	v_add_f32_e32 v33, v31, v33
	v_frexp_mant_f32_e32 v31, v32
	v_cvt_f64_f32_e32 v[42:43], v32
	v_cmp_gt_f32_e32 vcc, s19, v31
	v_frexp_exp_i32_f64_e32 v31, v[42:43]
	s_nop 0
	v_subbrev_co_u32_e32 v31, vcc, 0, v31, vcc
	v_sub_u32_e32 v42, 0, v31
	v_ldexp_f32 v32, v32, v42
	v_ldexp_f32 v33, v33, v42
	v_add_f32_e32 v42, -1.0, v32
	v_add_f32_e32 v43, 1.0, v42
	v_sub_f32_e32 v43, v32, v43
	v_add_f32_e32 v43, v33, v43
	v_add_f32_e32 v44, v42, v43
	v_sub_f32_e32 v42, v44, v42
	v_sub_f32_e32 v42, v43, v42
	v_add_f32_e32 v43, 1.0, v32
	v_add_f32_e32 v45, -1.0, v43
	v_sub_f32_e32 v32, v32, v45
	v_add_f32_e32 v32, v33, v32
	v_add_f32_e32 v33, v43, v32
	v_sub_f32_e32 v43, v33, v43
	v_sub_f32_e32 v32, v32, v43
	v_rcp_f32_e32 v43, v33
	v_cvt_f32_i32_e32 v31, v31
	v_cmp_neq_f32_e32 vcc, s27, v30
	v_mul_f32_e32 v45, v44, v43
	v_mul_f32_e32 v46, v33, v45
	v_fma_f32 v47, v45, v33, -v46
	v_fmac_f32_e32 v47, v45, v32
	v_add_f32_e32 v48, v46, v47
	v_sub_f32_e32 v49, v44, v48
	v_sub_f32_e32 v44, v44, v49
	v_sub_f32_e32 v46, v48, v46
	v_sub_f32_e32 v44, v44, v48
	v_add_f32_e32 v42, v42, v44
	v_sub_f32_e32 v44, v46, v47
	v_add_f32_e32 v42, v44, v42
	v_add_f32_e32 v44, v49, v42
	v_mul_f32_e32 v46, v43, v44
	v_mul_f32_e32 v47, v33, v46
	v_fma_f32 v33, v46, v33, -v47
	v_fmac_f32_e32 v33, v46, v32
	v_sub_f32_e32 v32, v49, v44
	v_add_f32_e32 v32, v42, v32
	v_add_f32_e32 v42, v47, v33
	v_sub_f32_e32 v48, v44, v42
	v_sub_f32_e32 v44, v44, v48
	v_sub_f32_e32 v47, v42, v47
	v_sub_f32_e32 v42, v44, v42
	v_add_f32_e32 v32, v32, v42
	v_sub_f32_e32 v33, v47, v33
	v_add_f32_e32 v32, v33, v32
	v_add_f32_e32 v33, v45, v46
	v_add_f32_e32 v32, v48, v32
	v_sub_f32_e32 v42, v33, v45
	v_mul_f32_e32 v32, v43, v32
	v_sub_f32_e32 v42, v46, v42
	v_add_f32_e32 v32, v42, v32
	v_mul_f32_e32 v45, 0x3f317218, v31
	v_add_f32_e32 v42, v33, v32
	v_fma_f32 v46, v31, s21, -v45
	v_mul_f32_e32 v43, v42, v42
	v_fmac_f32_e32 v46, 0xb102e308, v31
	v_sub_f32_e32 v31, v42, v33
	v_fmamk_f32 v44, v43, 0x3e9b6dac, v217
;     __device__ __forceinline__ void operator()(const f32x4 (&acc)[2][2][4][2], const Unit& u, int ui, int wr, int wc, int fr, int fq) const {
;     ...
;                             float z[6] = {y0[0], y0[1], y0[2], y0[3], y1[0], y1[1]};
; #pragma unroll
;                             for (int e = 0; e < 6; ++e) { const float zz = z[e] + bfg[e]; z[e] = fminf(zz, 0.f) - log1pf(__expf(-fabsf(zz))); }
;                             float* lp = (float*)(ws + E_LS) + (size_t)row;
; #pragma unroll
;                             for (int e = 0; e < 6; ++e) lp[(size_t)(e * 32768u)] = z[e];
	v_sub_f32_e32 v31, v32, v31
	v_add_f32_e32 v32, v45, v46
	v_fmaak_f32 v44, v43, v44, 0x3f2aaada
	v_sub_f32_e32 v33, v32, v45
	v_ldexp_f32 v45, v42, 1
	v_mul_f32_e32 v42, v42, v43
	v_mul_f32_e32 v42, v42, v44
	v_add_f32_e32 v43, v45, v42
	v_sub_f32_e32 v44, v43, v45
	v_ldexp_f32 v31, v31, 1
	v_sub_f32_e32 v42, v42, v44
	v_add_f32_e32 v31, v31, v42
	v_add_f32_e32 v42, v43, v31
	v_sub_f32_e32 v43, v42, v43
	v_sub_f32_e32 v31, v31, v43
	v_add_f32_e32 v43, v32, v42
	v_sub_f32_e32 v44, v43, v32
	v_sub_f32_e32 v45, v43, v44
	v_sub_f32_e32 v33, v46, v33
	v_sub_f32_e32 v32, v32, v45
	v_sub_f32_e32 v42, v42, v44
	v_add_f32_e32 v32, v42, v32
	v_add_f32_e32 v42, v33, v31
	v_sub_f32_e32 v44, v42, v33
	v_sub_f32_e32 v45, v42, v44
	v_sub_f32_e32 v33, v33, v45
	v_sub_f32_e32 v31, v31, v44
	v_add_f32_e32 v32, v42, v32
	v_add_f32_e32 v31, v31, v33
	v_add_f32_e32 v33, v43, v32
	v_sub_f32_e32 v42, v33, v43
	v_sub_f32_e32 v32, v32, v42
	v_add_f32_e32 v31, v31, v32
	v_add_f32_e32 v31, v33, v31
	v_cndmask_b32_e32 v31, v230, v31, vcc
	v_cmp_ngt_f32_e32 vcc, -1.0, v30
	s_nop 1
	v_cndmask_b32_e32 v31, v231, v31, vcc
	v_cmp_neq_f32_e32 vcc, -1.0, v30
	s_nop 1
	v_cndmask_b32_e32 v31, v226, v31, vcc
	v_cmp_lt_f32_e64 vcc, |v30|, s33
	s_nop 1
	v_cndmask_b32_e32 v30, v31, v30, vcc
	v_sub_f32_e32 v121, v29, v30
	v_mul_f32_e32 v114, v114, v26
	v_add_f32_e32 v30, v114, v14
	v_min_f32_e32 v29, 0, v30
	v_mul_f32_e64 v30, |v30|, s3
	v_exp_f32_e32 v30, v30
	s_nop 0
	v_add_f32_e32 v32, 1.0, v30
	v_add_f32_e32 v31, -1.0, v32
	v_sub_f32_e32 v33, v31, v32
	v_add_f32_e32 v33, 1.0, v33
	v_sub_f32_e32 v31, v30, v31
	v_add_f32_e32 v33, v31, v33
	v_frexp_mant_f32_e32 v31, v32
	v_cvt_f64_f32_e32 v[42:43], v32
	v_cmp_gt_f32_e32 vcc, s19, v31
	v_frexp_exp_i32_f64_e32 v31, v[42:43]
	s_nop 0
	v_subbrev_co_u32_e32 v31, vcc, 0, v31, vcc
	v_sub_u32_e32 v42, 0, v31
	v_ldexp_f32 v32, v32, v42
	v_ldexp_f32 v33, v33, v42
	v_add_f32_e32 v42, -1.0, v32
	v_add_f32_e32 v43, 1.0, v42
	v_sub_f32_e32 v43, v32, v43
	v_add_f32_e32 v43, v33, v43
	v_add_f32_e32 v44, v42, v43
	v_sub_f32_e32 v42, v44, v42
	v_sub_f32_e32 v42, v43, v42
	v_add_f32_e32 v43, 1.0, v32
	v_add_f32_e32 v45, -1.0, v43
	v_sub_f32_e32 v32, v32, v45
	v_add_f32_e32 v32, v33, v32
	v_add_f32_e32 v33, v43, v32
	v_sub_f32_e32 v43, v33, v43
	v_sub_f32_e32 v32, v32, v43
	v_rcp_f32_e32 v43, v33
	v_cvt_f32_i32_e32 v31, v31
	v_cmp_neq_f32_e32 vcc, s27, v30
	v_mul_f32_e32 v45, v44, v43
	v_mul_f32_e32 v46, v33, v45
	v_fma_f32 v47, v45, v33, -v46
	v_fmac_f32_e32 v47, v45, v32
	v_add_f32_e32 v48, v46, v47
	v_sub_f32_e32 v49, v44, v48
	v_sub_f32_e32 v44, v44, v49
	v_sub_f32_e32 v46, v48, v46
	v_sub_f32_e32 v44, v44, v48
	v_add_f32_e32 v42, v42, v44
	v_sub_f32_e32 v44, v46, v47
	v_add_f32_e32 v42, v44, v42
	v_add_f32_e32 v44, v49, v42
	v_mul_f32_e32 v46, v43, v44
	v_mul_f32_e32 v47, v33, v46
	v_fma_f32 v33, v46, v33, -v47
	v_fmac_f32_e32 v33, v46, v32
	v_sub_f32_e32 v32, v49, v44
	v_add_f32_e32 v32, v42, v32
	v_add_f32_e32 v42, v47, v33
	v_sub_f32_e32 v48, v44, v42
	v_sub_f32_e32 v44, v44, v48
	v_sub_f32_e32 v47, v42, v47
	v_sub_f32_e32 v42, v44, v42
	v_add_f32_e32 v32, v32, v42
	v_sub_f32_e32 v33, v47, v33
	v_add_f32_e32 v32, v33, v32
	v_add_f32_e32 v33, v45, v46
	v_add_f32_e32 v32, v48, v32
	v_sub_f32_e32 v42, v33, v45
	v_mul_f32_e32 v32, v43, v32
	v_sub_f32_e32 v42, v46, v42
	v_add_f32_e32 v32, v42, v32
	v_mul_f32_e32 v45, 0x3f317218, v31
	v_add_f32_e32 v42, v33, v32
	v_fma_f32 v46, v31, s21, -v45
	v_mul_f32_e32 v43, v42, v42
	v_fmac_f32_e32 v46, 0xb102e308, v31
	v_sub_f32_e32 v31, v42, v33
	v_fmamk_f32 v44, v43, 0x3e9b6dac, v217
	v_sub_f32_e32 v31, v32, v31
	v_add_f32_e32 v32, v45, v46
	v_fmaak_f32 v44, v43, v44, 0x3f2aaada
	v_sub_f32_e32 v33, v32, v45
	v_ldexp_f32 v45, v42, 1
	v_mul_f32_e32 v42, v42, v43
	v_mul_f32_e32 v42, v42, v44
	v_add_f32_e32 v43, v45, v42
	v_sub_f32_e32 v44, v43, v45
	v_ldexp_f32 v31, v31, 1
	v_sub_f32_e32 v42, v42, v44
	v_add_f32_e32 v31, v31, v42
	v_add_f32_e32 v42, v43, v31
	v_sub_f32_e32 v43, v42, v43
	v_sub_f32_e32 v31, v31, v43
	v_add_f32_e32 v43, v32, v42
	v_sub_f32_e32 v44, v43, v32
	v_sub_f32_e32 v45, v43, v44
	v_sub_f32_e32 v33, v46, v33
	v_sub_f32_e32 v32, v32, v45
	v_sub_f32_e32 v42, v42, v44
	v_add_f32_e32 v32, v42, v32
	v_add_f32_e32 v42, v33, v31
	v_sub_f32_e32 v44, v42, v33
	v_sub_f32_e32 v45, v42, v44
	v_sub_f32_e32 v33, v33, v45
	v_sub_f32_e32 v31, v31, v44
	v_add_f32_e32 v32, v42, v32
	v_add_f32_e32 v31, v31, v33
	v_add_f32_e32 v33, v43, v32
	v_sub_f32_e32 v42, v33, v43
	v_sub_f32_e32 v32, v32, v42
	v_add_f32_e32 v31, v31, v32
	v_add_f32_e32 v31, v33, v31
	v_cndmask_b32_e32 v31, v230, v31, vcc
	v_cmp_ngt_f32_e32 vcc, -1.0, v30
	s_nop 1
	v_cndmask_b32_e32 v31, v231, v31, vcc
	v_cmp_neq_f32_e32 vcc, -1.0, v30
	s_nop 1
	v_cndmask_b32_e32 v31, v226, v31, vcc
	v_cmp_lt_f32_e64 vcc, |v30|, s33
	s_nop 1
	v_cndmask_b32_e32 v30, v31, v30, vcc
	v_sub_f32_e32 v114, v29, v30
	v_mul_f32_e32 v115, v115, v26
	v_add_f32_e32 v30, v115, v15
	v_min_f32_e32 v29, 0, v30
	v_mul_f32_e64 v30, |v30|, s3
	v_exp_f32_e32 v30, v30
	s_nop 0
	v_add_f32_e32 v32, 1.0, v30
	v_add_f32_e32 v31, -1.0, v32
	v_sub_f32_e32 v33, v31, v32
	v_add_f32_e32 v33, 1.0, v33
	v_sub_f32_e32 v31, v30, v31
	v_add_f32_e32 v33, v31, v33
	v_frexp_mant_f32_e32 v31, v32
	v_cvt_f64_f32_e32 v[42:43], v32
	v_cmp_gt_f32_e32 vcc, s19, v31
	v_frexp_exp_i32_f64_e32 v31, v[42:43]
	s_nop 0
	v_subbrev_co_u32_e32 v31, vcc, 0, v31, vcc
	v_sub_u32_e32 v42, 0, v31
	v_ldexp_f32 v32, v32, v42
	v_ldexp_f32 v33, v33, v42
	v_add_f32_e32 v42, -1.0, v32
	v_add_f32_e32 v43, 1.0, v42
	v_sub_f32_e32 v43, v32, v43
	v_add_f32_e32 v43, v33, v43
	v_add_f32_e32 v44, v42, v43
;     __device__ __forceinline__ void operator()(const f32x4 (&acc)[2][2][4][2], const Unit& u, int ui, int wr, int wc, int fr, int fq) const {
;     ...
;                             float z[6] = {y0[0], y0[1], y0[2], y0[3], y1[0], y1[1]};
; #pragma unroll
;                             for (int e = 0; e < 6; ++e) { const float zz = z[e] + bfg[e]; z[e] = fminf(zz, 0.f) - log1pf(__expf(-fabsf(zz))); }
;                             float* lp = (float*)(ws + E_LS) + (size_t)row;
; #pragma unroll
;                             for (int e = 0; e < 6; ++e) lp[(size_t)(e * 32768u)] = z[e];
	v_sub_f32_e32 v42, v44, v42
	v_sub_f32_e32 v42, v43, v42
	v_add_f32_e32 v43, 1.0, v32
	v_add_f32_e32 v45, -1.0, v43
	v_sub_f32_e32 v32, v32, v45
	v_add_f32_e32 v32, v33, v32
	v_add_f32_e32 v33, v43, v32
	v_sub_f32_e32 v43, v33, v43
	v_sub_f32_e32 v32, v32, v43
	v_rcp_f32_e32 v43, v33
	v_cvt_f32_i32_e32 v31, v31
	v_cmp_neq_f32_e32 vcc, s27, v30
	v_mul_f32_e32 v45, v44, v43
	v_mul_f32_e32 v46, v33, v45
	v_fma_f32 v47, v45, v33, -v46
	v_fmac_f32_e32 v47, v45, v32
	v_add_f32_e32 v48, v46, v47
	v_sub_f32_e32 v49, v44, v48
	v_sub_f32_e32 v44, v44, v49
	v_sub_f32_e32 v46, v48, v46
	v_sub_f32_e32 v44, v44, v48
	v_add_f32_e32 v42, v42, v44
	v_sub_f32_e32 v44, v46, v47
	v_add_f32_e32 v42, v44, v42
	v_add_f32_e32 v44, v49, v42
	v_mul_f32_e32 v46, v43, v44
	v_mul_f32_e32 v47, v33, v46
	v_fma_f32 v33, v46, v33, -v47
	v_fmac_f32_e32 v33, v46, v32
	v_sub_f32_e32 v32, v49, v44
	v_add_f32_e32 v32, v42, v32
	v_add_f32_e32 v42, v47, v33
	v_sub_f32_e32 v48, v44, v42
	v_sub_f32_e32 v44, v44, v48
	v_sub_f32_e32 v47, v42, v47
	v_sub_f32_e32 v42, v44, v42
	v_add_f32_e32 v32, v32, v42
	v_sub_f32_e32 v33, v47, v33
	v_add_f32_e32 v32, v33, v32
	v_add_f32_e32 v33, v45, v46
	v_add_f32_e32 v32, v48, v32
	v_sub_f32_e32 v42, v33, v45
	v_mul_f32_e32 v32, v43, v32
	v_sub_f32_e32 v42, v46, v42
	v_add_f32_e32 v32, v42, v32
	v_mul_f32_e32 v45, 0x3f317218, v31
	v_add_f32_e32 v42, v33, v32
	v_fma_f32 v46, v31, s21, -v45
	v_mul_f32_e32 v43, v42, v42
	v_fmac_f32_e32 v46, 0xb102e308, v31
	v_sub_f32_e32 v31, v42, v33
	v_fmamk_f32 v44, v43, 0x3e9b6dac, v217
	v_sub_f32_e32 v31, v32, v31
	v_add_f32_e32 v32, v45, v46
	v_fmaak_f32 v44, v43, v44, 0x3f2aaada
	v_sub_f32_e32 v33, v32, v45
	v_ldexp_f32 v45, v42, 1
	v_mul_f32_e32 v42, v42, v43
	v_mul_f32_e32 v42, v42, v44
	v_add_f32_e32 v43, v45, v42
	v_sub_f32_e32 v44, v43, v45
	v_ldexp_f32 v31, v31, 1
	v_sub_f32_e32 v42, v42, v44
	v_add_f32_e32 v31, v31, v42
	v_add_f32_e32 v42, v43, v31
	v_sub_f32_e32 v43, v42, v43
	v_sub_f32_e32 v31, v31, v43
	v_add_f32_e32 v43, v32, v42
	v_sub_f32_e32 v44, v43, v32
	v_sub_f32_e32 v45, v43, v44
	v_sub_f32_e32 v33, v46, v33
	v_sub_f32_e32 v32, v32, v45
	v_sub_f32_e32 v42, v42, v44
	v_add_f32_e32 v32, v42, v32
	v_add_f32_e32 v42, v33, v31
	v_sub_f32_e32 v44, v42, v33
	v_sub_f32_e32 v45, v42, v44
	v_sub_f32_e32 v33, v33, v45
	v_sub_f32_e32 v31, v31, v44
	v_add_f32_e32 v32, v42, v32
	v_add_f32_e32 v31, v31, v33
	v_add_f32_e32 v33, v43, v32
	v_sub_f32_e32 v42, v33, v43
	v_sub_f32_e32 v32, v32, v42
	v_add_f32_e32 v31, v31, v32
	v_add_f32_e32 v31, v33, v31
	v_cndmask_b32_e32 v31, v230, v31, vcc
	v_cmp_ngt_f32_e32 vcc, -1.0, v30
	s_nop 1
	v_cndmask_b32_e32 v31, v231, v31, vcc
	v_cmp_neq_f32_e32 vcc, -1.0, v30
	s_nop 1
	v_cndmask_b32_e32 v31, v226, v31, vcc
	v_cmp_lt_f32_e64 vcc, |v30|, s33
	s_nop 1
	v_cndmask_b32_e32 v30, v31, v30, vcc
	v_sub_f32_e32 v115, v29, v30
	v_mul_f32_e32 v102, v102, v27
	v_add_f32_e32 v30, v102, v10
	v_min_f32_e32 v29, 0, v30
	v_mul_f32_e64 v30, |v30|, s3
	v_exp_f32_e32 v30, v30
	s_nop 0
	v_add_f32_e32 v32, 1.0, v30
	v_add_f32_e32 v31, -1.0, v32
	v_sub_f32_e32 v33, v31, v32
	v_add_f32_e32 v33, 1.0, v33
	v_sub_f32_e32 v31, v30, v31
	v_add_f32_e32 v33, v31, v33
	v_frexp_mant_f32_e32 v31, v32
	v_cvt_f64_f32_e32 v[42:43], v32
	v_cmp_gt_f32_e32 vcc, s19, v31
	v_frexp_exp_i32_f64_e32 v31, v[42:43]
	s_nop 0
	v_subbrev_co_u32_e32 v31, vcc, 0, v31, vcc
	v_sub_u32_e32 v42, 0, v31
	v_ldexp_f32 v32, v32, v42
	v_ldexp_f32 v33, v33, v42
	v_add_f32_e32 v42, -1.0, v32
	v_add_f32_e32 v43, 1.0, v42
	v_sub_f32_e32 v43, v32, v43
	v_add_f32_e32 v43, v33, v43
	v_add_f32_e32 v44, v42, v43
	v_sub_f32_e32 v42, v44, v42
	v_sub_f32_e32 v42, v43, v42
	v_add_f32_e32 v43, 1.0, v32
	v_add_f32_e32 v45, -1.0, v43
	v_sub_f32_e32 v32, v32, v45
	v_add_f32_e32 v32, v33, v32
	v_add_f32_e32 v33, v43, v32
	v_sub_f32_e32 v43, v33, v43
	v_sub_f32_e32 v32, v32, v43
	v_rcp_f32_e32 v43, v33
	v_cvt_f32_i32_e32 v31, v31
	v_cmp_neq_f32_e32 vcc, s27, v30
	v_mul_f32_e32 v45, v44, v43
	v_mul_f32_e32 v46, v33, v45
	v_fma_f32 v47, v45, v33, -v46
	v_fmac_f32_e32 v47, v45, v32
	v_add_f32_e32 v48, v46, v47
	v_sub_f32_e32 v49, v44, v48
	v_sub_f32_e32 v44, v44, v49
	v_sub_f32_e32 v46, v48, v46
	v_sub_f32_e32 v44, v44, v48
	v_add_f32_e32 v42, v42, v44
	v_sub_f32_e32 v44, v46, v47
	v_add_f32_e32 v42, v44, v42
	v_add_f32_e32 v44, v49, v42
	v_mul_f32_e32 v46, v43, v44
	v_mul_f32_e32 v47, v33, v46
	v_fma_f32 v33, v46, v33, -v47
	v_fmac_f32_e32 v33, v46, v32
	v_sub_f32_e32 v32, v49, v44
	v_add_f32_e32 v32, v42, v32
	v_add_f32_e32 v42, v47, v33
	v_sub_f32_e32 v48, v44, v42
	v_sub_f32_e32 v44, v44, v48
	v_sub_f32_e32 v47, v42, v47
	v_sub_f32_e32 v42, v44, v42
	v_add_f32_e32 v32, v32, v42
	v_sub_f32_e32 v33, v47, v33
	v_add_f32_e32 v32, v33, v32
	v_add_f32_e32 v33, v45, v46
	v_add_f32_e32 v32, v48, v32
	v_sub_f32_e32 v42, v33, v45
	v_mul_f32_e32 v32, v43, v32
	v_sub_f32_e32 v42, v46, v42
	v_add_f32_e32 v32, v42, v32
	v_mul_f32_e32 v45, 0x3f317218, v31
	v_add_f32_e32 v42, v33, v32
	v_fma_f32 v46, v31, s21, -v45
	v_mul_f32_e32 v43, v42, v42
	v_fmac_f32_e32 v46, 0xb102e308, v31
	v_sub_f32_e32 v31, v42, v33
	v_fmamk_f32 v44, v43, 0x3e9b6dac, v217
	v_sub_f32_e32 v31, v32, v31
	v_add_f32_e32 v32, v45, v46
	v_fmaak_f32 v44, v43, v44, 0x3f2aaada
	v_sub_f32_e32 v33, v32, v45
	v_ldexp_f32 v45, v42, 1
	v_mul_f32_e32 v42, v42, v43
	v_mul_f32_e32 v42, v42, v44
	v_add_f32_e32 v43, v45, v42
	v_sub_f32_e32 v44, v43, v45
	v_ldexp_f32 v31, v31, 1
	v_sub_f32_e32 v42, v42, v44
	v_add_f32_e32 v31, v31, v42
	v_add_f32_e32 v42, v43, v31
	v_sub_f32_e32 v43, v42, v43
	v_sub_f32_e32 v31, v31, v43
	v_add_f32_e32 v43, v32, v42
	v_sub_f32_e32 v44, v43, v32
	v_sub_f32_e32 v45, v43, v44
;     __device__ __forceinline__ void operator()(const f32x4 (&acc)[2][2][4][2], const Unit& u, int ui, int wr, int wc, int fr, int fq) const {
;     ...
;                             float z[6] = {y0[0], y0[1], y0[2], y0[3], y1[0], y1[1]};
; #pragma unroll
;                             for (int e = 0; e < 6; ++e) { const float zz = z[e] + bfg[e]; z[e] = fminf(zz, 0.f) - log1pf(__expf(-fabsf(zz))); }
;                             float* lp = (float*)(ws + E_LS) + (size_t)row;
; #pragma unroll
;                             for (int e = 0; e < 6; ++e) lp[(size_t)(e * 32768u)] = z[e];
	v_sub_f32_e32 v33, v46, v33
	v_sub_f32_e32 v32, v32, v45
	v_sub_f32_e32 v42, v42, v44
	v_add_f32_e32 v32, v42, v32
	v_add_f32_e32 v42, v33, v31
	v_sub_f32_e32 v44, v42, v33
	v_sub_f32_e32 v45, v42, v44
	v_sub_f32_e32 v33, v33, v45
	v_sub_f32_e32 v31, v31, v44
	v_add_f32_e32 v32, v42, v32
	v_add_f32_e32 v31, v31, v33
	v_add_f32_e32 v33, v43, v32
	v_sub_f32_e32 v42, v33, v43
	v_sub_f32_e32 v32, v32, v42
	v_add_f32_e32 v31, v31, v32
	v_add_f32_e32 v31, v33, v31
	v_cndmask_b32_e32 v31, v230, v31, vcc
	v_cmp_ngt_f32_e32 vcc, -1.0, v30
	s_nop 1
	v_cndmask_b32_e32 v31, v231, v31, vcc
	v_cmp_neq_f32_e32 vcc, -1.0, v30
	s_nop 1
	v_cndmask_b32_e32 v31, v226, v31, vcc
	v_cmp_lt_f32_e64 vcc, |v30|, s33
	s_nop 1
	v_cndmask_b32_e32 v30, v31, v30, vcc
	v_sub_f32_e32 v102, v29, v30
	v_mul_f32_e32 v103, v103, v27
	v_add_f32_e32 v30, v103, v11
	v_min_f32_e32 v29, 0, v30
	v_mul_f32_e64 v30, |v30|, s3
	v_exp_f32_e32 v30, v30
	s_nop 0
	v_add_f32_e32 v32, 1.0, v30
	v_add_f32_e32 v31, -1.0, v32
	v_sub_f32_e32 v33, v31, v32
	v_add_f32_e32 v33, 1.0, v33
	v_sub_f32_e32 v31, v30, v31
	v_add_f32_e32 v33, v31, v33
	v_frexp_mant_f32_e32 v31, v32
	v_cvt_f64_f32_e32 v[42:43], v32
	v_cmp_gt_f32_e32 vcc, s19, v31
	v_frexp_exp_i32_f64_e32 v31, v[42:43]
	s_nop 0
	v_subbrev_co_u32_e32 v31, vcc, 0, v31, vcc
	v_sub_u32_e32 v42, 0, v31
	v_ldexp_f32 v32, v32, v42
	v_ldexp_f32 v33, v33, v42
	v_add_f32_e32 v42, -1.0, v32
	v_add_f32_e32 v43, 1.0, v42
	v_sub_f32_e32 v43, v32, v43
	v_add_f32_e32 v43, v33, v43
	v_add_f32_e32 v44, v42, v43
	v_sub_f32_e32 v42, v44, v42
	v_sub_f32_e32 v42, v43, v42
	v_add_f32_e32 v43, 1.0, v32
	v_add_f32_e32 v45, -1.0, v43
	v_sub_f32_e32 v32, v32, v45
	v_add_f32_e32 v32, v33, v32
	v_add_f32_e32 v33, v43, v32
	v_sub_f32_e32 v43, v33, v43
	v_sub_f32_e32 v32, v32, v43
	v_rcp_f32_e32 v43, v33
	v_cvt_f32_i32_e32 v31, v31
	v_cmp_neq_f32_e32 vcc, s27, v30
	v_mul_f32_e32 v45, v44, v43
	v_mul_f32_e32 v46, v33, v45
	v_fma_f32 v47, v45, v33, -v46
	v_fmac_f32_e32 v47, v45, v32
	v_add_f32_e32 v48, v46, v47
	v_sub_f32_e32 v49, v44, v48
	v_sub_f32_e32 v44, v44, v49
	v_sub_f32_e32 v46, v48, v46
	v_sub_f32_e32 v44, v44, v48
	v_add_f32_e32 v42, v42, v44
	v_sub_f32_e32 v44, v46, v47
	v_add_f32_e32 v42, v44, v42
	v_add_f32_e32 v44, v49, v42
	v_mul_f32_e32 v46, v43, v44
	v_mul_f32_e32 v47, v33, v46
	v_fma_f32 v33, v46, v33, -v47
	v_fmac_f32_e32 v33, v46, v32
	v_sub_f32_e32 v32, v49, v44
	v_add_f32_e32 v32, v42, v32
	v_add_f32_e32 v42, v47, v33
	v_sub_f32_e32 v48, v44, v42
	v_sub_f32_e32 v44, v44, v48
	v_sub_f32_e32 v47, v42, v47
	v_sub_f32_e32 v42, v44, v42
	v_add_f32_e32 v32, v32, v42
	v_sub_f32_e32 v33, v47, v33
	v_add_f32_e32 v32, v33, v32
	v_add_f32_e32 v33, v45, v46
	v_add_f32_e32 v32, v48, v32
	v_sub_f32_e32 v42, v33, v45
	v_mul_f32_e32 v32, v43, v32
	v_sub_f32_e32 v42, v46, v42
	v_add_f32_e32 v32, v42, v32
	v_mul_f32_e32 v45, 0x3f317218, v31
	v_add_f32_e32 v42, v33, v32
	v_fma_f32 v46, v31, s21, -v45
	v_mul_f32_e32 v43, v42, v42
	v_fmac_f32_e32 v46, 0xb102e308, v31
	v_sub_f32_e32 v31, v42, v33
	v_fmamk_f32 v44, v43, 0x3e9b6dac, v217
	v_sub_f32_e32 v31, v32, v31
	v_add_f32_e32 v32, v45, v46
	v_fmaak_f32 v44, v43, v44, 0x3f2aaada
	v_sub_f32_e32 v33, v32, v45
	v_ldexp_f32 v45, v42, 1
	v_mul_f32_e32 v42, v42, v43
	v_mul_f32_e32 v42, v42, v44
	v_add_f32_e32 v43, v45, v42
	v_sub_f32_e32 v44, v43, v45
	v_ldexp_f32 v31, v31, 1
	v_sub_f32_e32 v42, v42, v44
	v_add_f32_e32 v31, v31, v42
	v_add_f32_e32 v42, v43, v31
	v_sub_f32_e32 v43, v42, v43
	v_sub_f32_e32 v31, v31, v43
	v_add_f32_e32 v43, v32, v42
	v_sub_f32_e32 v44, v43, v32
	v_sub_f32_e32 v45, v43, v44
	v_sub_f32_e32 v33, v46, v33
	v_sub_f32_e32 v32, v32, v45
	v_sub_f32_e32 v42, v42, v44
	v_add_f32_e32 v32, v42, v32
	v_add_f32_e32 v42, v33, v31
	v_sub_f32_e32 v44, v42, v33
	v_sub_f32_e32 v45, v42, v44
	v_sub_f32_e32 v33, v33, v45
	v_sub_f32_e32 v31, v31, v44
	v_add_f32_e32 v32, v42, v32
	v_add_f32_e32 v31, v31, v33
	v_add_f32_e32 v33, v43, v32
	v_sub_f32_e32 v42, v33, v43
	v_sub_f32_e32 v32, v32, v42
	v_add_f32_e32 v31, v31, v32
	v_add_f32_e32 v31, v33, v31
	v_cndmask_b32_e32 v31, v230, v31, vcc
	v_cmp_ngt_f32_e32 vcc, -1.0, v30
	s_nop 1
	v_cndmask_b32_e32 v31, v231, v31, vcc
	v_cmp_neq_f32_e32 vcc, -1.0, v30
	s_nop 1
	v_cndmask_b32_e32 v31, v226, v31, vcc
	v_cmp_lt_f32_e64 vcc, |v30|, s33
	s_nop 1
	v_cndmask_b32_e32 v30, v31, v30, vcc
	v_sub_f32_e32 v103, v29, v30
	v_mul_f32_e32 v104, v104, v27
	v_add_f32_e32 v30, v104, v12
	v_min_f32_e32 v29, 0, v30
	v_mul_f32_e64 v30, |v30|, s3
	v_exp_f32_e32 v30, v30
	s_nop 0
	v_add_f32_e32 v32, 1.0, v30
	v_add_f32_e32 v31, -1.0, v32
	v_sub_f32_e32 v33, v31, v32
	v_add_f32_e32 v33, 1.0, v33
	v_sub_f32_e32 v31, v30, v31
	v_add_f32_e32 v33, v31, v33
	v_frexp_mant_f32_e32 v31, v32
	v_cvt_f64_f32_e32 v[42:43], v32
	v_cmp_gt_f32_e32 vcc, s19, v31
	v_frexp_exp_i32_f64_e32 v31, v[42:43]
	s_nop 0
	v_subbrev_co_u32_e32 v31, vcc, 0, v31, vcc
	v_sub_u32_e32 v42, 0, v31
	v_ldexp_f32 v32, v32, v42
	v_ldexp_f32 v33, v33, v42
	v_add_f32_e32 v42, -1.0, v32
	v_add_f32_e32 v43, 1.0, v42
	v_sub_f32_e32 v43, v32, v43
	v_add_f32_e32 v43, v33, v43
	v_add_f32_e32 v44, v42, v43
	v_sub_f32_e32 v42, v44, v42
	v_sub_f32_e32 v42, v43, v42
	v_add_f32_e32 v43, 1.0, v32
	v_add_f32_e32 v45, -1.0, v43
	v_sub_f32_e32 v32, v32, v45
	v_add_f32_e32 v32, v33, v32
	v_add_f32_e32 v33, v43, v32
	v_sub_f32_e32 v43, v33, v43
	v_sub_f32_e32 v32, v32, v43
	v_rcp_f32_e32 v43, v33
	v_cvt_f32_i32_e32 v31, v31
	v_cmp_neq_f32_e32 vcc, s27, v30
	v_mul_f32_e32 v45, v44, v43
	v_mul_f32_e32 v46, v33, v45
	v_fma_f32 v47, v45, v33, -v46
	v_fmac_f32_e32 v47, v45, v32
	v_add_f32_e32 v48, v46, v47
	v_sub_f32_e32 v49, v44, v48
;     __device__ __forceinline__ void operator()(const f32x4 (&acc)[2][2][4][2], const Unit& u, int ui, int wr, int wc, int fr, int fq) const {
;     ...
;                             float z[6] = {y0[0], y0[1], y0[2], y0[3], y1[0], y1[1]};
; #pragma unroll
;                             for (int e = 0; e < 6; ++e) { const float zz = z[e] + bfg[e]; z[e] = fminf(zz, 0.f) - log1pf(__expf(-fabsf(zz))); }
	v_sub_f32_e32 v44, v44, v49
	v_sub_f32_e32 v46, v48, v46
	v_sub_f32_e32 v44, v44, v48
	v_add_f32_e32 v42, v42, v44
	v_sub_f32_e32 v44, v46, v47
	v_add_f32_e32 v42, v44, v42
	v_add_f32_e32 v44, v49, v42
	v_mul_f32_e32 v46, v43, v44
	v_mul_f32_e32 v47, v33, v46
	v_fma_f32 v33, v46, v33, -v47
	v_fmac_f32_e32 v33, v46, v32
	v_sub_f32_e32 v32, v49, v44
	v_add_f32_e32 v32, v42, v32
	v_add_f32_e32 v42, v47, v33
	v_sub_f32_e32 v48, v44, v42
	v_sub_f32_e32 v44, v44, v48
	v_sub_f32_e32 v47, v42, v47
	v_sub_f32_e32 v42, v44, v42
	v_add_f32_e32 v32, v32, v42
	v_sub_f32_e32 v33, v47, v33
	v_add_f32_e32 v32, v33, v32
	v_add_f32_e32 v33, v45, v46
	v_add_f32_e32 v32, v48, v32
	v_sub_f32_e32 v42, v33, v45
	v_mul_f32_e32 v32, v43, v32
	v_sub_f32_e32 v42, v46, v42
	v_add_f32_e32 v32, v42, v32
	v_mul_f32_e32 v45, 0x3f317218, v31
	v_add_f32_e32 v42, v33, v32
	v_fma_f32 v46, v31, s21, -v45
	v_mul_f32_e32 v43, v42, v42
	v_fmac_f32_e32 v46, 0xb102e308, v31
	v_sub_f32_e32 v31, v42, v33
	v_fmamk_f32 v44, v43, 0x3e9b6dac, v217
	v_sub_f32_e32 v31, v32, v31
	v_add_f32_e32 v32, v45, v46
	v_fmaak_f32 v44, v43, v44, 0x3f2aaada
	v_sub_f32_e32 v33, v32, v45
	v_ldexp_f32 v45, v42, 1
	v_mul_f32_e32 v42, v42, v43
	v_mul_f32_e32 v42, v42, v44
	v_add_f32_e32 v43, v45, v42
	v_sub_f32_e32 v44, v43, v45
	v_ldexp_f32 v31, v31, 1
	v_sub_f32_e32 v42, v42, v44
	v_add_f32_e32 v31, v31, v42
	v_add_f32_e32 v42, v43, v31
	v_sub_f32_e32 v43, v42, v43
	v_sub_f32_e32 v31, v31, v43
	v_add_f32_e32 v43, v32, v42
	v_sub_f32_e32 v44, v43, v32
	v_sub_f32_e32 v45, v43, v44
	v_sub_f32_e32 v33, v46, v33
	v_sub_f32_e32 v32, v32, v45
	v_sub_f32_e32 v42, v42, v44
	v_add_f32_e32 v32, v42, v32
	v_add_f32_e32 v42, v33, v31
	v_sub_f32_e32 v44, v42, v33
	v_sub_f32_e32 v45, v42, v44
	v_sub_f32_e32 v33, v33, v45
	v_sub_f32_e32 v31, v31, v44
	v_add_f32_e32 v32, v42, v32
	v_add_f32_e32 v31, v31, v33
	v_add_f32_e32 v33, v43, v32
	v_sub_f32_e32 v42, v33, v43
	v_sub_f32_e32 v32, v32, v42
	v_add_f32_e32 v31, v31, v32
	v_add_f32_e32 v31, v33, v31
	v_cndmask_b32_e32 v31, v230, v31, vcc
	v_cmp_ngt_f32_e32 vcc, -1.0, v30
	s_nop 1
	v_cndmask_b32_e32 v31, v231, v31, vcc
	v_cmp_neq_f32_e32 vcc, -1.0, v30
	s_nop 1
	v_cndmask_b32_e32 v31, v226, v31, vcc
	v_cmp_lt_f32_e64 vcc, |v30|, s33
	s_nop 1
	v_cndmask_b32_e32 v30, v31, v30, vcc
	v_sub_f32_e32 v104, v29, v30
	v_mul_f32_e32 v105, v105, v27
	v_add_f32_e32 v30, v105, v13
	v_min_f32_e32 v29, 0, v30
	v_mul_f32_e64 v30, |v30|, s3
	v_exp_f32_e32 v30, v30
	s_nop 0
	v_add_f32_e32 v32, 1.0, v30
	v_add_f32_e32 v31, -1.0, v32
	v_sub_f32_e32 v33, v31, v32
	v_add_f32_e32 v33, 1.0, v33
	v_sub_f32_e32 v31, v30, v31
	v_add_f32_e32 v33, v31, v33
	v_frexp_mant_f32_e32 v31, v32
	v_cvt_f64_f32_e32 v[42:43], v32
	v_cmp_gt_f32_e32 vcc, s19, v31
	v_frexp_exp_i32_f64_e32 v31, v[42:43]
	s_nop 0
	v_subbrev_co_u32_e32 v31, vcc, 0, v31, vcc
	v_sub_u32_e32 v42, 0, v31
	v_ldexp_f32 v32, v32, v42
	v_ldexp_f32 v33, v33, v42
	v_add_f32_e32 v42, -1.0, v32
	v_add_f32_e32 v43, 1.0, v42
	v_sub_f32_e32 v43, v32, v43
	v_add_f32_e32 v43, v33, v43
	v_add_f32_e32 v44, v42, v43
	v_sub_f32_e32 v42, v44, v42
	v_sub_f32_e32 v42, v43, v42
	v_add_f32_e32 v43, 1.0, v32
	v_add_f32_e32 v45, -1.0, v43
	v_sub_f32_e32 v32, v32, v45
	v_add_f32_e32 v32, v33, v32
	v_add_f32_e32 v33, v43, v32
	v_sub_f32_e32 v43, v33, v43
	v_sub_f32_e32 v32, v32, v43
	v_rcp_f32_e32 v43, v33
	v_cvt_f32_i32_e32 v31, v31
	v_cmp_neq_f32_e32 vcc, s27, v30
	v_mul_f32_e32 v45, v44, v43
	v_mul_f32_e32 v46, v33, v45
	v_fma_f32 v47, v45, v33, -v46
	v_fmac_f32_e32 v47, v45, v32
	v_add_f32_e32 v48, v46, v47
	v_sub_f32_e32 v49, v44, v48
	v_sub_f32_e32 v44, v44, v49
	v_sub_f32_e32 v46, v48, v46
	v_sub_f32_e32 v44, v44, v48
	v_add_f32_e32 v42, v42, v44
	v_sub_f32_e32 v44, v46, v47
	v_add_f32_e32 v42, v44, v42
	v_add_f32_e32 v44, v49, v42
	v_mul_f32_e32 v46, v43, v44
	v_mul_f32_e32 v47, v33, v46
	v_fma_f32 v33, v46, v33, -v47
	v_fmac_f32_e32 v33, v46, v32
	v_sub_f32_e32 v32, v49, v44
	v_add_f32_e32 v32, v42, v32
	v_add_f32_e32 v42, v47, v33
	v_sub_f32_e32 v48, v44, v42
	v_sub_f32_e32 v44, v44, v48
	v_sub_f32_e32 v47, v42, v47
	v_sub_f32_e32 v42, v44, v42
	v_add_f32_e32 v32, v32, v42
	v_sub_f32_e32 v33, v47, v33
	v_add_f32_e32 v32, v33, v32
	v_add_f32_e32 v33, v45, v46
	v_add_f32_e32 v32, v48, v32
	v_sub_f32_e32 v42, v33, v45
	v_mul_f32_e32 v32, v43, v32
	v_sub_f32_e32 v42, v46, v42
	v_add_f32_e32 v32, v42, v32
	v_mul_f32_e32 v45, 0x3f317218, v31
	v_add_f32_e32 v42, v33, v32
	v_fma_f32 v46, v31, s21, -v45
	v_mul_f32_e32 v43, v42, v42
	v_fmac_f32_e32 v46, 0xb102e308, v31
	v_sub_f32_e32 v31, v42, v33
	v_fmamk_f32 v44, v43, 0x3e9b6dac, v217
	v_sub_f32_e32 v31, v32, v31
	v_add_f32_e32 v32, v45, v46
	v_fmaak_f32 v44, v43, v44, 0x3f2aaada
	v_sub_f32_e32 v33, v32, v45
	v_ldexp_f32 v45, v42, 1
	v_mul_f32_e32 v42, v42, v43
	v_mul_f32_e32 v42, v42, v44
	v_add_f32_e32 v43, v45, v42
	v_sub_f32_e32 v44, v43, v45
	v_ldexp_f32 v31, v31, 1
	v_sub_f32_e32 v42, v42, v44
	v_add_f32_e32 v31, v31, v42
	v_add_f32_e32 v42, v43, v31
	v_sub_f32_e32 v43, v42, v43
	v_sub_f32_e32 v31, v31, v43
	v_add_f32_e32 v43, v32, v42
	v_sub_f32_e32 v44, v43, v32
	v_sub_f32_e32 v45, v43, v44
	v_sub_f32_e32 v33, v46, v33
	v_sub_f32_e32 v32, v32, v45
	v_sub_f32_e32 v42, v42, v44
	v_add_f32_e32 v32, v42, v32
	v_add_f32_e32 v42, v33, v31
	v_sub_f32_e32 v44, v42, v33
	v_sub_f32_e32 v45, v42, v44
	v_sub_f32_e32 v33, v33, v45
	v_sub_f32_e32 v31, v31, v44
	v_add_f32_e32 v32, v42, v32
	v_add_f32_e32 v31, v31, v33
	v_add_f32_e32 v33, v43, v32
	v_sub_f32_e32 v42, v33, v43
	v_sub_f32_e32 v32, v32, v42
	v_add_f32_e32 v31, v31, v32
	v_add_f32_e32 v31, v33, v31
	v_cndmask_b32_e32 v31, v230, v31, vcc
;     __device__ __forceinline__ void operator()(const f32x4 (&acc)[2][2][4][2], const Unit& u, int ui, int wr, int wc, int fr, int fq) const {
;     ...
;                             float z[6] = {y0[0], y0[1], y0[2], y0[3], y1[0], y1[1]};
; #pragma unroll
;                             for (int e = 0; e < 6; ++e) { const float zz = z[e] + bfg[e]; z[e] = fminf(zz, 0.f) - log1pf(__expf(-fabsf(zz))); }
	v_cmp_ngt_f32_e32 vcc, -1.0, v30
	s_nop 1
	v_cndmask_b32_e32 v31, v231, v31, vcc
	v_cmp_neq_f32_e32 vcc, -1.0, v30
	s_nop 1
	v_cndmask_b32_e32 v31, v226, v31, vcc
	v_cmp_lt_f32_e64 vcc, |v30|, s33
	s_nop 1
	v_cndmask_b32_e32 v30, v31, v30, vcc
	v_sub_f32_e32 v105, v29, v30
	v_mul_f32_e32 v98, v98, v27
	v_add_f32_e32 v30, v98, v14
	v_min_f32_e32 v29, 0, v30
	v_mul_f32_e64 v30, |v30|, s3
	v_exp_f32_e32 v30, v30
	s_nop 0
	v_add_f32_e32 v32, 1.0, v30
	v_add_f32_e32 v31, -1.0, v32
	v_sub_f32_e32 v33, v31, v32
	v_add_f32_e32 v33, 1.0, v33
	v_sub_f32_e32 v31, v30, v31
	v_add_f32_e32 v33, v31, v33
	v_frexp_mant_f32_e32 v31, v32
	v_cvt_f64_f32_e32 v[42:43], v32
	v_cmp_gt_f32_e32 vcc, s19, v31
	v_frexp_exp_i32_f64_e32 v31, v[42:43]
	s_nop 0
	v_subbrev_co_u32_e32 v31, vcc, 0, v31, vcc
	v_sub_u32_e32 v42, 0, v31
	v_ldexp_f32 v32, v32, v42
	v_ldexp_f32 v33, v33, v42
	v_add_f32_e32 v42, -1.0, v32
	v_add_f32_e32 v43, 1.0, v42
	v_sub_f32_e32 v43, v32, v43
	v_add_f32_e32 v43, v33, v43
	v_add_f32_e32 v44, v42, v43
	v_sub_f32_e32 v42, v44, v42
	v_sub_f32_e32 v42, v43, v42
	v_add_f32_e32 v43, 1.0, v32
	v_add_f32_e32 v45, -1.0, v43
	v_sub_f32_e32 v32, v32, v45
	v_add_f32_e32 v32, v33, v32
	v_add_f32_e32 v33, v43, v32
	v_sub_f32_e32 v43, v33, v43
	v_sub_f32_e32 v32, v32, v43
	v_rcp_f32_e32 v43, v33
	v_cvt_f32_i32_e32 v31, v31
	v_cmp_neq_f32_e32 vcc, s27, v30
	v_mul_f32_e32 v45, v44, v43
	v_mul_f32_e32 v46, v33, v45
	v_fma_f32 v47, v45, v33, -v46
	v_fmac_f32_e32 v47, v45, v32
	v_add_f32_e32 v48, v46, v47
	v_sub_f32_e32 v49, v44, v48
	v_sub_f32_e32 v44, v44, v49
	v_sub_f32_e32 v46, v48, v46
	v_sub_f32_e32 v44, v44, v48
	v_add_f32_e32 v42, v42, v44
	v_sub_f32_e32 v44, v46, v47
	v_add_f32_e32 v42, v44, v42
	v_add_f32_e32 v44, v49, v42
	v_mul_f32_e32 v46, v43, v44
	v_mul_f32_e32 v47, v33, v46
	v_fma_f32 v33, v46, v33, -v47
	v_fmac_f32_e32 v33, v46, v32
	v_sub_f32_e32 v32, v49, v44
	v_add_f32_e32 v32, v42, v32
	v_add_f32_e32 v42, v47, v33
	v_sub_f32_e32 v48, v44, v42
	v_sub_f32_e32 v44, v44, v48
	v_sub_f32_e32 v47, v42, v47
	v_sub_f32_e32 v42, v44, v42
	v_add_f32_e32 v32, v32, v42
	v_sub_f32_e32 v33, v47, v33
	v_add_f32_e32 v32, v33, v32
	v_add_f32_e32 v33, v45, v46
	v_add_f32_e32 v32, v48, v32
	v_sub_f32_e32 v42, v33, v45
	v_mul_f32_e32 v32, v43, v32
	v_sub_f32_e32 v42, v46, v42
	v_add_f32_e32 v32, v42, v32
	v_mul_f32_e32 v45, 0x3f317218, v31
	v_add_f32_e32 v42, v33, v32
	v_fma_f32 v46, v31, s21, -v45
	v_mul_f32_e32 v43, v42, v42
	v_fmac_f32_e32 v46, 0xb102e308, v31
	v_sub_f32_e32 v31, v42, v33
	v_fmamk_f32 v44, v43, 0x3e9b6dac, v217
	v_sub_f32_e32 v31, v32, v31
	v_add_f32_e32 v32, v45, v46
	v_fmaak_f32 v44, v43, v44, 0x3f2aaada
	v_sub_f32_e32 v33, v32, v45
	v_ldexp_f32 v45, v42, 1
	v_mul_f32_e32 v42, v42, v43
	v_mul_f32_e32 v42, v42, v44
	v_add_f32_e32 v43, v45, v42
	v_sub_f32_e32 v44, v43, v45
	v_ldexp_f32 v31, v31, 1
	v_sub_f32_e32 v42, v42, v44
	v_add_f32_e32 v31, v31, v42
	v_add_f32_e32 v42, v43, v31
	v_sub_f32_e32 v43, v42, v43
	v_sub_f32_e32 v31, v31, v43
	v_add_f32_e32 v43, v32, v42
	v_sub_f32_e32 v44, v43, v32
	v_sub_f32_e32 v45, v43, v44
	v_sub_f32_e32 v33, v46, v33
	v_sub_f32_e32 v32, v32, v45
	v_sub_f32_e32 v42, v42, v44
	v_add_f32_e32 v32, v42, v32
	v_add_f32_e32 v42, v33, v31
	v_sub_f32_e32 v44, v42, v33
	v_sub_f32_e32 v45, v42, v44
	v_sub_f32_e32 v33, v33, v45
	v_sub_f32_e32 v31, v31, v44
	v_add_f32_e32 v32, v42, v32
	v_add_f32_e32 v31, v31, v33
	v_add_f32_e32 v33, v43, v32
	v_sub_f32_e32 v42, v33, v43
	v_sub_f32_e32 v32, v32, v42
	v_add_f32_e32 v31, v31, v32
	v_add_f32_e32 v31, v33, v31
	v_cndmask_b32_e32 v31, v230, v31, vcc
	v_cmp_ngt_f32_e32 vcc, -1.0, v30
	s_nop 1
	v_cndmask_b32_e32 v31, v231, v31, vcc
	v_cmp_neq_f32_e32 vcc, -1.0, v30
	s_nop 1
	v_cndmask_b32_e32 v31, v226, v31, vcc
	v_cmp_lt_f32_e64 vcc, |v30|, s33
	s_nop 1
	v_cndmask_b32_e32 v30, v31, v30, vcc
	v_sub_f32_e32 v98, v29, v30
	v_mul_f32_e32 v99, v99, v27
	v_add_f32_e32 v30, v99, v15
	v_min_f32_e32 v29, 0, v30
	v_mul_f32_e64 v30, |v30|, s3
	v_exp_f32_e32 v30, v30
	s_nop 0
	v_add_f32_e32 v32, 1.0, v30
	v_add_f32_e32 v31, -1.0, v32
	v_sub_f32_e32 v33, v31, v32
	v_add_f32_e32 v33, 1.0, v33
	v_sub_f32_e32 v31, v30, v31
	v_add_f32_e32 v33, v31, v33
;     __device__ __forceinline__ void operator()(const f32x4 (&acc)[2][2][4][2], const Unit& u, int ui, int wr, int wc, int fr, int fq) const {
;     ...
;                             for (int e = 0; e < 6; ++e) { const float zz = z[e] + bfg[e]; z[e] = fminf(zz, 0.f) - log1pf(__expf(-fabsf(zz))); }
;                             float* lp = (float*)(ws + E_LS) + (size_t)row;
; #pragma unroll
;                             for (int e = 0; e < 6; ++e) lp[(size_t)(e * 32768u)] = z[e];
	v_frexp_mant_f32_e32 v31, v32
	v_cvt_f64_f32_e32 v[42:43], v32
	v_cmp_gt_f32_e32 vcc, s19, v31
	v_frexp_exp_i32_f64_e32 v31, v[42:43]
	s_nop 0
	v_subbrev_co_u32_e32 v31, vcc, 0, v31, vcc
	v_sub_u32_e32 v42, 0, v31
	v_ldexp_f32 v32, v32, v42
	v_ldexp_f32 v33, v33, v42
	v_add_f32_e32 v42, -1.0, v32
	v_add_f32_e32 v43, 1.0, v42
	v_sub_f32_e32 v43, v32, v43
	v_add_f32_e32 v43, v33, v43
	v_add_f32_e32 v44, v42, v43
	v_sub_f32_e32 v42, v44, v42
	v_sub_f32_e32 v42, v43, v42
	v_add_f32_e32 v43, 1.0, v32
	v_add_f32_e32 v45, -1.0, v43
	v_sub_f32_e32 v32, v32, v45
	v_add_f32_e32 v32, v33, v32
	v_add_f32_e32 v33, v43, v32
	v_sub_f32_e32 v43, v33, v43
	v_sub_f32_e32 v32, v32, v43
	v_rcp_f32_e32 v43, v33
	v_cvt_f32_i32_e32 v31, v31
	v_cmp_neq_f32_e32 vcc, s27, v30
	v_mul_f32_e32 v45, v44, v43
	v_mul_f32_e32 v46, v33, v45
	v_fma_f32 v47, v45, v33, -v46
	v_fmac_f32_e32 v47, v45, v32
	v_add_f32_e32 v48, v46, v47
	v_sub_f32_e32 v49, v44, v48
	v_sub_f32_e32 v44, v44, v49
	v_sub_f32_e32 v46, v48, v46
	v_sub_f32_e32 v44, v44, v48
	v_add_f32_e32 v42, v42, v44
	v_sub_f32_e32 v44, v46, v47
	v_add_f32_e32 v42, v44, v42
	v_add_f32_e32 v44, v49, v42
	v_mul_f32_e32 v46, v43, v44
	v_mul_f32_e32 v47, v33, v46
	v_fma_f32 v33, v46, v33, -v47
	v_fmac_f32_e32 v33, v46, v32
	v_sub_f32_e32 v32, v49, v44
	v_add_f32_e32 v32, v42, v32
	v_add_f32_e32 v42, v47, v33
	v_sub_f32_e32 v48, v44, v42
	v_sub_f32_e32 v44, v44, v48
	v_sub_f32_e32 v47, v42, v47
	v_sub_f32_e32 v42, v44, v42
	v_add_f32_e32 v32, v32, v42
	v_sub_f32_e32 v33, v47, v33
	v_add_f32_e32 v32, v33, v32
	v_add_f32_e32 v33, v45, v46
	v_add_f32_e32 v32, v48, v32
	v_sub_f32_e32 v42, v33, v45
	v_mul_f32_e32 v32, v43, v32
	v_sub_f32_e32 v42, v46, v42
	v_add_f32_e32 v32, v42, v32
	v_mul_f32_e32 v45, 0x3f317218, v31
	v_add_f32_e32 v42, v33, v32
	v_fma_f32 v46, v31, s21, -v45
	v_mul_f32_e32 v43, v42, v42
	v_fmac_f32_e32 v46, 0xb102e308, v31
	v_sub_f32_e32 v31, v42, v33
	v_fmamk_f32 v44, v43, 0x3e9b6dac, v217
	v_sub_f32_e32 v31, v32, v31
	v_add_f32_e32 v32, v45, v46
	v_fmaak_f32 v44, v43, v44, 0x3f2aaada
	v_sub_f32_e32 v33, v32, v45
	v_ldexp_f32 v45, v42, 1
	v_mul_f32_e32 v42, v42, v43
	v_mul_f32_e32 v42, v42, v44
	v_add_f32_e32 v43, v45, v42
	v_sub_f32_e32 v44, v43, v45
	v_ldexp_f32 v31, v31, 1
	v_sub_f32_e32 v42, v42, v44
	v_add_f32_e32 v31, v31, v42
	v_add_f32_e32 v42, v43, v31
	v_sub_f32_e32 v43, v42, v43
	v_sub_f32_e32 v31, v31, v43
	v_add_f32_e32 v43, v32, v42
	v_sub_f32_e32 v44, v43, v32
	v_sub_f32_e32 v45, v43, v44
	v_sub_f32_e32 v33, v46, v33
	v_sub_f32_e32 v32, v32, v45
	v_sub_f32_e32 v42, v42, v44
	v_add_f32_e32 v32, v42, v32
	v_add_f32_e32 v42, v33, v31
	v_sub_f32_e32 v44, v42, v33
	v_sub_f32_e32 v45, v42, v44
	v_sub_f32_e32 v33, v33, v45
	v_sub_f32_e32 v31, v31, v44
	v_add_f32_e32 v32, v42, v32
	v_add_f32_e32 v31, v31, v33
	v_add_f32_e32 v33, v43, v32
	v_sub_f32_e32 v42, v33, v43
	v_sub_f32_e32 v32, v32, v42
	v_add_f32_e32 v31, v31, v32
	v_add_f32_e32 v31, v33, v31
	v_cndmask_b32_e32 v31, v230, v31, vcc
	v_cmp_ngt_f32_e32 vcc, -1.0, v30
	s_nop 1
	v_cndmask_b32_e32 v31, v231, v31, vcc
	v_cmp_neq_f32_e32 vcc, -1.0, v30
	s_nop 1
	v_cndmask_b32_e32 v31, v226, v31, vcc
	v_cmp_lt_f32_e64 vcc, |v30|, s33
	s_nop 1
	v_cndmask_b32_e32 v30, v31, v30, vcc
	v_sub_f32_e32 v99, v29, v30
	s_mov_b64 s[30:31], s[12:13]
	global_store_dword v28, v118, s[30:31]
	global_store_dword v28, v102, s[30:31] offset:64
	s_add_u32 s30, s30, 0x20000
	s_addc_u32 s31, s31, 0
	global_store_dword v28, v119, s[30:31]
	global_store_dword v28, v103, s[30:31] offset:64
	s_add_u32 s30, s30, 0x20000
	s_addc_u32 s31, s31, 0
	global_store_dword v28, v120, s[30:31]
	global_store_dword v28, v104, s[30:31] offset:64
	s_add_u32 s30, s30, 0x20000
	s_addc_u32 s31, s31, 0
	global_store_dword v28, v121, s[30:31]
	global_store_dword v28, v105, s[30:31] offset:64
	s_add_u32 s30, s30, 0x20000
	s_addc_u32 s31, s31, 0
	global_store_dword v28, v114, s[30:31]
	global_store_dword v28, v98, s[30:31] offset:64
	s_add_u32 s30, s30, 0x20000
	s_addc_u32 s31, s31, 0
	global_store_dword v28, v115, s[30:31]
	global_store_dword v28, v99, s[30:31] offset:64
.Lflg_done:
	s_and_saveexec_b64 s[28:29], s[34:35]
	s_cbranch_execz .LBB0_606
